# hand-written scan loader (wave = 8-step quarter, all streams, lane = k pair) pre-scales kk/kka/kt/r by the cumulative decay of each 4-step group; scanner applies W once per 4 steps; same f32 math reas
# speedup vs baseline: 1.0133x; 1.0133x over previous
.LBB0_607:
	s_mul_i32 s33, s8, 0xab
	s_bfe_u32 s33, s33, 0x70009
	s_mul_i32 s33, s33, 3
	s_sub_i32 s33, s8, s33
	s_and_b32 s33, s33, 0xff
	s_mul_i32 s33, s33, 0xa800
	s_add_i32 s33, s33, 0
	s_waitcnt vmcnt(0)
	v_add_u32_e32 v19, s33, v96
	v_add_u32_e32 v18, s33, v87
	v_add_u32_e32 v2, 0xa000, v19
	v_add_u32_e32 v3, 0xa400, v19
	ds_read_b128 v[20:23], v18
	ds_read_b128 v[32:35], v18 offset:24576
	ds_read2_b32 v[80:81], v2 offset1:16
	ds_read_b128 v[24:27], v18 offset:8192
	ds_read_b128 v[36:39], v18 offset:32768
	ds_read_b128 v[40:43], v18 offset:256
	ds_read_b128 v[52:55], v18 offset:24832
	ds_read_b128 v[44:47], v18 offset:8448
	ds_read_b128 v[56:59], v18 offset:33024
	s_ashr_i32 s47, s46, 31
	s_lshl_b64 s[46:47], s[46:47], 9
	v_lshl_add_u64 v[12:13], v[10:11], 0, s[46:47]
	s_waitcnt lgkmcnt(5)
	v_pk_mul_f32 v[104:105], v[14:15], v[20:21]
	s_nop 0
	v_pk_fma_f32 v[104:105], v[16:17], v[22:23], v[104:105]
	s_nop 0
	v_add_f32_e32 v102, v104, v105
	v_pk_fma_f32 v[14:15], v[32:33], v[80:81], v[14:15] op_sel_hi:[1,0,1]
	ds_read_b128 v[60:63], v18 offset:512
	v_add_f32_dpp v102, v102, v102 quad_perm:[1,0,3,2] row_mask:0xf bank_mask:0xf bound_ctrl:1
	v_pk_fma_f32 v[16:17], v[34:35], v[80:81], v[16:17] op_sel_hi:[1,0,1]
	ds_read_b128 v[72:75], v18 offset:25088
	v_add_f32_dpp v102, v102, v102 quad_perm:[2,3,0,1] row_mask:0xf bank_mask:0xf bound_ctrl:1
	ds_read_b128 v[64:67], v18 offset:8704
	ds_read_b128 v[76:79], v18 offset:33280
	v_add_f32_dpp v102, v102, v102 row_half_mirror row_mask:0xf bank_mask:0xf bound_ctrl:1
	ds_read2_b32 v[92:93], v2 offset0:32 offset1:48
	s_nop 0
	v_add_f32_dpp v102, v102, v102 row_mirror row_mask:0xf bank_mask:0xf bound_ctrl:1
	v_pk_fma_f32 v[14:15], v[24:25], v[102:103], v[14:15] op_sel_hi:[1,0,1] neg_lo:[0,1,0] neg_hi:[0,1,0]
	v_pk_fma_f32 v[16:17], v[26:27], v[102:103], v[16:17] op_sel_hi:[1,0,1] neg_lo:[0,1,0] neg_hi:[0,1,0]
	s_waitcnt lgkmcnt(6)
	v_pk_mul_f32 v[104:105], v[14:15], v[40:41]
	v_pk_mul_f32 v[106:107], v[14:15], v[36:37]
	v_pk_fma_f32 v[104:105], v[16:17], v[42:43], v[104:105]
	v_pk_fma_f32 v[106:107], v[16:17], v[38:39], v[106:107]
	v_add_f32_e32 v102, v104, v105
	v_pk_fma_f32 v[14:15], v[52:53], v[80:81], v[14:15] op_sel:[0,1,0]
	v_add_f32_e32 v112, v106, v107
	v_add_f32_dpp v102, v102, v102 quad_perm:[1,0,3,2] row_mask:0xf bank_mask:0xf bound_ctrl:1
	v_pk_fma_f32 v[16:17], v[54:55], v[80:81], v[16:17] op_sel:[0,1,0]
	ds_read_b128 v[20:23], v18 offset:768
	v_add_f32_dpp v102, v102, v102 quad_perm:[2,3,0,1] row_mask:0xf bank_mask:0xf bound_ctrl:1
	ds_read_b128 v[32:35], v18 offset:25344
	ds_read_b128 v[24:27], v18 offset:8960
	v_add_f32_dpp v102, v102, v102 row_half_mirror row_mask:0xf bank_mask:0xf bound_ctrl:1
	ds_read_b128 v[36:39], v18 offset:33536
	ds_read_b128 v[28:31], v18 offset:17152
	v_add_f32_dpp v102, v102, v102 row_mirror row_mask:0xf bank_mask:0xf bound_ctrl:1
	v_pk_fma_f32 v[14:15], v[44:45], v[102:103], v[14:15] op_sel_hi:[1,0,1] neg_lo:[0,1,0] neg_hi:[0,1,0]
	v_pk_fma_f32 v[16:17], v[46:47], v[102:103], v[16:17] op_sel_hi:[1,0,1] neg_lo:[0,1,0] neg_hi:[0,1,0]
	s_waitcnt lgkmcnt(7)
	v_pk_mul_f32 v[104:105], v[14:15], v[60:61]
	v_pk_mul_f32 v[106:107], v[14:15], v[56:57]
	v_pk_fma_f32 v[104:105], v[16:17], v[62:63], v[104:105]
	v_pk_fma_f32 v[106:107], v[16:17], v[58:59], v[106:107]
	v_add_f32_e32 v102, v104, v105
	s_waitcnt lgkmcnt(5)
	v_pk_fma_f32 v[14:15], v[72:73], v[92:93], v[14:15] op_sel_hi:[1,0,1]
	v_add_f32_e32 v113, v106, v107
	v_add_f32_dpp v102, v102, v102 quad_perm:[1,0,3,2] row_mask:0xf bank_mask:0xf bound_ctrl:1
	v_pk_fma_f32 v[16:17], v[74:75], v[92:93], v[16:17] op_sel_hi:[1,0,1]
	ds_read_b128 v[40:43], v18 offset:1024
	v_add_f32_dpp v102, v102, v102 quad_perm:[2,3,0,1] row_mask:0xf bank_mask:0xf bound_ctrl:1
	ds_read_b128 v[52:55], v18 offset:25600
	ds_read_b128 v[44:47], v18 offset:9216
	v_add_f32_dpp v102, v102, v102 row_half_mirror row_mask:0xf bank_mask:0xf bound_ctrl:1
	ds_read_b128 v[56:59], v18 offset:33792
	ds_read2_b32 v[80:81], v2 offset0:64 offset1:80
	v_add_f32_dpp v102, v102, v102 row_mirror row_mask:0xf bank_mask:0xf bound_ctrl:1
	v_pk_fma_f32 v[14:15], v[64:65], v[102:103], v[14:15] op_sel_hi:[1,0,1] neg_lo:[0,1,0] neg_hi:[0,1,0]
	v_pk_fma_f32 v[16:17], v[66:67], v[102:103], v[16:17] op_sel_hi:[1,0,1] neg_lo:[0,1,0] neg_hi:[0,1,0]
	v_add_f32_dpp v114, v112, v112 row_mirror row_mask:0xf bank_mask:0x3 bound_ctrl:1
	v_add_f32_dpp v114, v113, v113 row_mirror row_mask:0xf bank_mask:0xc bound_ctrl:1
	s_waitcnt lgkmcnt(7)
	v_pk_mul_f32 v[104:105], v[14:15], v[20:21]
	v_pk_mul_f32 v[106:107], v[14:15], v[76:77]
	v_pk_fma_f32 v[104:105], v[16:17], v[22:23], v[104:105]
	v_pk_fma_f32 v[106:107], v[16:17], v[78:79], v[106:107]
	v_add_f32_e32 v102, v104, v105
	v_pk_fma_f32 v[14:15], v[32:33], v[92:93], v[14:15] op_sel:[0,1,0]
	v_add_f32_e32 v112, v106, v107
	v_add_f32_dpp v102, v102, v102 quad_perm:[1,0,3,2] row_mask:0xf bank_mask:0xf bound_ctrl:1
	v_pk_fma_f32 v[16:17], v[34:35], v[92:93], v[16:17] op_sel:[0,1,0]
	ds_read_b128 v[60:63], v18 offset:1280
	v_add_f32_dpp v102, v102, v102 quad_perm:[2,3,0,1] row_mask:0xf bank_mask:0xf bound_ctrl:1
	ds_read_b128 v[72:75], v18 offset:25856
	ds_read_b128 v[64:67], v18 offset:9472
	v_add_f32_dpp v102, v102, v102 row_half_mirror row_mask:0xf bank_mask:0xf bound_ctrl:1
	ds_read_b128 v[76:79], v18 offset:34048
	s_nop 0
	v_add_f32_dpp v102, v102, v102 row_mirror row_mask:0xf bank_mask:0xf bound_ctrl:1
	v_pk_fma_f32 v[14:15], v[24:25], v[102:103], v[14:15] op_sel_hi:[1,0,1] neg_lo:[0,1,0] neg_hi:[0,1,0]
	v_pk_fma_f32 v[16:17], v[26:27], v[102:103], v[16:17] op_sel_hi:[1,0,1] neg_lo:[0,1,0] neg_hi:[0,1,0]
	s_waitcnt lgkmcnt(9)
	v_pk_mul_f32 v[14:15], v[14:15], v[28:29]
	v_pk_mul_f32 v[16:17], v[16:17], v[30:31]
	s_waitcnt lgkmcnt(6)
	v_pk_mul_f32 v[104:105], v[14:15], v[40:41]
	v_pk_mul_f32 v[106:107], v[14:15], v[36:37]
	v_pk_fma_f32 v[104:105], v[16:17], v[42:43], v[104:105]
	v_pk_fma_f32 v[106:107], v[16:17], v[38:39], v[106:107]
	v_add_f32_e32 v102, v104, v105
	s_waitcnt lgkmcnt(4)
	v_pk_fma_f32 v[14:15], v[52:53], v[80:81], v[14:15] op_sel_hi:[1,0,1]
	v_add_f32_e32 v113, v106, v107
	v_add_f32_dpp v102, v102, v102 quad_perm:[1,0,3,2] row_mask:0xf bank_mask:0xf bound_ctrl:1
	v_pk_fma_f32 v[16:17], v[54:55], v[80:81], v[16:17] op_sel_hi:[1,0,1]
	ds_read_b128 v[20:23], v18 offset:1536
	v_add_f32_dpp v102, v102, v102 quad_perm:[2,3,0,1] row_mask:0xf bank_mask:0xf bound_ctrl:1
	ds_read_b128 v[32:35], v18 offset:26112
	ds_read_b128 v[24:27], v18 offset:9728
	v_add_f32_dpp v102, v102, v102 row_half_mirror row_mask:0xf bank_mask:0xf bound_ctrl:1
	ds_read_b128 v[36:39], v18 offset:34304
	ds_read2_b32 v[92:93], v2 offset0:96 offset1:112
	v_add_f32_dpp v102, v102, v102 row_mirror row_mask:0xf bank_mask:0xf bound_ctrl:1
	v_pk_fma_f32 v[14:15], v[44:45], v[102:103], v[14:15] op_sel_hi:[1,0,1] neg_lo:[0,1,0] neg_hi:[0,1,0]
	v_pk_fma_f32 v[16:17], v[46:47], v[102:103], v[16:17] op_sel_hi:[1,0,1] neg_lo:[0,1,0] neg_hi:[0,1,0]
	v_add_f32_dpp v115, v112, v112 row_mirror row_mask:0xf bank_mask:0x3 bound_ctrl:1
	v_add_f32_dpp v115, v113, v113 row_mirror row_mask:0xf bank_mask:0xc bound_ctrl:1
	v_add_f32_dpp v116, v114, v114 row_half_mirror row_mask:0xf bank_mask:0x5 bound_ctrl:1
	s_nop 0
	v_add_f32_dpp v116, v115, v115 row_half_mirror row_mask:0xf bank_mask:0xa bound_ctrl:1
	s_waitcnt lgkmcnt(6)
	v_pk_mul_f32 v[104:105], v[14:15], v[60:61]
	v_pk_mul_f32 v[106:107], v[14:15], v[56:57]
	v_pk_fma_f32 v[104:105], v[16:17], v[62:63], v[104:105]
	v_pk_fma_f32 v[106:107], v[16:17], v[58:59], v[106:107]
	v_add_f32_e32 v102, v104, v105
	v_pk_fma_f32 v[14:15], v[72:73], v[80:81], v[14:15] op_sel:[0,1,0]
	v_add_f32_e32 v112, v106, v107
	v_add_f32_dpp v102, v102, v102 quad_perm:[1,0,3,2] row_mask:0xf bank_mask:0xf bound_ctrl:1
	v_pk_fma_f32 v[16:17], v[74:75], v[80:81], v[16:17] op_sel:[0,1,0]
	ds_read_b128 v[40:43], v18 offset:1792
	v_add_f32_dpp v102, v102, v102 quad_perm:[2,3,0,1] row_mask:0xf bank_mask:0xf bound_ctrl:1
	ds_read_b128 v[52:55], v18 offset:26368
	ds_read_b128 v[44:47], v18 offset:9984
	v_add_f32_dpp v102, v102, v102 row_half_mirror row_mask:0xf bank_mask:0xf bound_ctrl:1
	ds_read_b128 v[56:59], v18 offset:34560
	ds_read_b128 v[48:51], v18 offset:18176
	v_add_f32_dpp v102, v102, v102 row_mirror row_mask:0xf bank_mask:0xf bound_ctrl:1
	v_pk_fma_f32 v[14:15], v[64:65], v[102:103], v[14:15] op_sel_hi:[1,0,1] neg_lo:[0,1,0] neg_hi:[0,1,0]
	v_pk_fma_f32 v[16:17], v[66:67], v[102:103], v[16:17] op_sel_hi:[1,0,1] neg_lo:[0,1,0] neg_hi:[0,1,0]
	s_waitcnt lgkmcnt(7)
	v_pk_mul_f32 v[104:105], v[14:15], v[20:21]
	v_pk_mul_f32 v[106:107], v[14:15], v[76:77]
	v_pk_fma_f32 v[104:105], v[16:17], v[22:23], v[104:105]
	v_pk_fma_f32 v[106:107], v[16:17], v[78:79], v[106:107]
	v_add_f32_e32 v102, v104, v105
	s_waitcnt lgkmcnt(5)
	v_pk_fma_f32 v[14:15], v[32:33], v[92:93], v[14:15] op_sel_hi:[1,0,1]
	v_add_f32_e32 v113, v106, v107
	v_add_f32_dpp v102, v102, v102 quad_perm:[1,0,3,2] row_mask:0xf bank_mask:0xf bound_ctrl:1
	v_pk_fma_f32 v[16:17], v[34:35], v[92:93], v[16:17] op_sel_hi:[1,0,1]
	ds_read_b128 v[60:63], v18 offset:2048
	v_add_f32_dpp v102, v102, v102 quad_perm:[2,3,0,1] row_mask:0xf bank_mask:0xf bound_ctrl:1
	ds_read_b128 v[72:75], v18 offset:26624
	ds_read_b128 v[64:67], v18 offset:10240
	v_add_f32_dpp v102, v102, v102 row_half_mirror row_mask:0xf bank_mask:0xf bound_ctrl:1
	ds_read_b128 v[76:79], v18 offset:34816
	ds_read2_b32 v[80:81], v2 offset0:128 offset1:144
	v_add_f32_dpp v102, v102, v102 row_mirror row_mask:0xf bank_mask:0xf bound_ctrl:1
	v_pk_fma_f32 v[14:15], v[24:25], v[102:103], v[14:15] op_sel_hi:[1,0,1] neg_lo:[0,1,0] neg_hi:[0,1,0]
	v_pk_fma_f32 v[16:17], v[26:27], v[102:103], v[16:17] op_sel_hi:[1,0,1] neg_lo:[0,1,0] neg_hi:[0,1,0]
	v_add_f32_dpp v114, v112, v112 row_mirror row_mask:0xf bank_mask:0x3 bound_ctrl:1
	v_add_f32_dpp v114, v113, v113 row_mirror row_mask:0xf bank_mask:0xc bound_ctrl:1
	s_waitcnt lgkmcnt(7)
	v_pk_mul_f32 v[104:105], v[14:15], v[40:41]
	v_pk_mul_f32 v[106:107], v[14:15], v[36:37]
	v_pk_fma_f32 v[104:105], v[16:17], v[42:43], v[104:105]
	v_pk_fma_f32 v[106:107], v[16:17], v[38:39], v[106:107]
	v_add_f32_e32 v102, v104, v105
	v_pk_fma_f32 v[14:15], v[52:53], v[92:93], v[14:15] op_sel:[0,1,0]
	v_add_f32_e32 v112, v106, v107
	v_add_f32_dpp v102, v102, v102 quad_perm:[1,0,3,2] row_mask:0xf bank_mask:0xf bound_ctrl:1
	v_pk_fma_f32 v[16:17], v[54:55], v[92:93], v[16:17] op_sel:[0,1,0]
	ds_read_b128 v[20:23], v18 offset:2304
	v_add_f32_dpp v102, v102, v102 quad_perm:[2,3,0,1] row_mask:0xf bank_mask:0xf bound_ctrl:1
	ds_read_b128 v[32:35], v18 offset:26880
	ds_read_b128 v[24:27], v18 offset:10496
	v_add_f32_dpp v102, v102, v102 row_half_mirror row_mask:0xf bank_mask:0xf bound_ctrl:1
	ds_read_b128 v[36:39], v18 offset:35072
	s_nop 0
	v_add_f32_dpp v102, v102, v102 row_mirror row_mask:0xf bank_mask:0xf bound_ctrl:1
	v_pk_fma_f32 v[14:15], v[44:45], v[102:103], v[14:15] op_sel_hi:[1,0,1] neg_lo:[0,1,0] neg_hi:[0,1,0]
	v_pk_fma_f32 v[16:17], v[46:47], v[102:103], v[16:17] op_sel_hi:[1,0,1] neg_lo:[0,1,0] neg_hi:[0,1,0]
	s_waitcnt lgkmcnt(9)
	v_pk_mul_f32 v[14:15], v[14:15], v[48:49]
	v_pk_mul_f32 v[16:17], v[16:17], v[50:51]
	s_waitcnt lgkmcnt(6)
	v_pk_mul_f32 v[104:105], v[14:15], v[60:61]
	v_pk_mul_f32 v[106:107], v[14:15], v[56:57]
	v_pk_fma_f32 v[104:105], v[16:17], v[62:63], v[104:105]
	v_pk_fma_f32 v[106:107], v[16:17], v[58:59], v[106:107]
	v_add_f32_e32 v102, v104, v105
	s_waitcnt lgkmcnt(4)
	v_pk_fma_f32 v[14:15], v[72:73], v[80:81], v[14:15] op_sel_hi:[1,0,1]
	v_add_f32_e32 v113, v106, v107
	v_add_f32_dpp v102, v102, v102 quad_perm:[1,0,3,2] row_mask:0xf bank_mask:0xf bound_ctrl:1
	v_pk_fma_f32 v[16:17], v[74:75], v[80:81], v[16:17] op_sel_hi:[1,0,1]
	ds_read_b128 v[40:43], v18 offset:2560
	v_add_f32_dpp v102, v102, v102 quad_perm:[2,3,0,1] row_mask:0xf bank_mask:0xf bound_ctrl:1
	ds_read_b128 v[52:55], v18 offset:27136
	ds_read_b128 v[44:47], v18 offset:10752
	v_add_f32_dpp v102, v102, v102 row_half_mirror row_mask:0xf bank_mask:0xf bound_ctrl:1
	ds_read_b128 v[56:59], v18 offset:35328
	ds_read2_b32 v[92:93], v2 offset0:160 offset1:176
	v_add_f32_dpp v102, v102, v102 row_mirror row_mask:0xf bank_mask:0xf bound_ctrl:1
	v_pk_fma_f32 v[14:15], v[64:65], v[102:103], v[14:15] op_sel_hi:[1,0,1] neg_lo:[0,1,0] neg_hi:[0,1,0]
	v_pk_fma_f32 v[16:17], v[66:67], v[102:103], v[16:17] op_sel_hi:[1,0,1] neg_lo:[0,1,0] neg_hi:[0,1,0]
	v_add_f32_dpp v115, v112, v112 row_mirror row_mask:0xf bank_mask:0x3 bound_ctrl:1
	v_add_f32_dpp v115, v113, v113 row_mirror row_mask:0xf bank_mask:0xc bound_ctrl:1
	v_add_f32_dpp v117, v114, v114 row_half_mirror row_mask:0xf bank_mask:0x5 bound_ctrl:1
	s_nop 0
	v_add_f32_dpp v117, v115, v115 row_half_mirror row_mask:0xf bank_mask:0xa bound_ctrl:1
	v_add_f32_dpp v120, v116, v116 quad_perm:[2,3,0,1] row_mask:0xf bank_mask:0xf bound_ctrl:1
	s_nop 0
	v_add_f32_dpp v121, v117, v117 quad_perm:[2,3,0,1] row_mask:0xf bank_mask:0xf bound_ctrl:1
	s_waitcnt lgkmcnt(6)
	v_pk_mul_f32 v[104:105], v[14:15], v[20:21]
	v_pk_mul_f32 v[106:107], v[14:15], v[76:77]
	v_pk_fma_f32 v[104:105], v[16:17], v[22:23], v[104:105]
	v_pk_fma_f32 v[106:107], v[16:17], v[78:79], v[106:107]
	v_add_f32_e32 v102, v104, v105
	v_pk_fma_f32 v[14:15], v[32:33], v[80:81], v[14:15] op_sel:[0,1,0]
	v_add_f32_e32 v112, v106, v107
	v_add_f32_dpp v102, v102, v102 quad_perm:[1,0,3,2] row_mask:0xf bank_mask:0xf bound_ctrl:1
	v_pk_fma_f32 v[16:17], v[34:35], v[80:81], v[16:17] op_sel:[0,1,0]
	ds_read_b128 v[60:63], v18 offset:2816
	v_add_f32_dpp v102, v102, v102 quad_perm:[2,3,0,1] row_mask:0xf bank_mask:0xf bound_ctrl:1
	ds_read_b128 v[72:75], v18 offset:27392
	ds_read_b128 v[64:67], v18 offset:11008
	v_add_f32_dpp v102, v102, v102 row_half_mirror row_mask:0xf bank_mask:0xf bound_ctrl:1
	ds_read_b128 v[76:79], v18 offset:35584
	ds_read_b128 v[68:71], v18 offset:19200
	v_add_f32_dpp v102, v102, v102 row_mirror row_mask:0xf bank_mask:0xf bound_ctrl:1
	v_pk_fma_f32 v[14:15], v[24:25], v[102:103], v[14:15] op_sel_hi:[1,0,1] neg_lo:[0,1,0] neg_hi:[0,1,0]
	v_pk_fma_f32 v[16:17], v[26:27], v[102:103], v[16:17] op_sel_hi:[1,0,1] neg_lo:[0,1,0] neg_hi:[0,1,0]
	v_cndmask_b32_e64 v118, v120, v121, s[14:15]
	s_waitcnt lgkmcnt(7)
	v_pk_mul_f32 v[104:105], v[14:15], v[40:41]
	v_pk_mul_f32 v[106:107], v[14:15], v[36:37]
	v_pk_fma_f32 v[104:105], v[16:17], v[42:43], v[104:105]
	v_pk_fma_f32 v[106:107], v[16:17], v[38:39], v[106:107]
	v_add_f32_e32 v102, v104, v105
	s_waitcnt lgkmcnt(5)
	v_pk_fma_f32 v[14:15], v[52:53], v[92:93], v[14:15] op_sel_hi:[1,0,1]
	v_add_f32_e32 v113, v106, v107
	v_add_f32_dpp v102, v102, v102 quad_perm:[1,0,3,2] row_mask:0xf bank_mask:0xf bound_ctrl:1
	v_pk_fma_f32 v[16:17], v[54:55], v[92:93], v[16:17] op_sel_hi:[1,0,1]
	ds_read_b128 v[20:23], v18 offset:3072
	v_add_f32_dpp v102, v102, v102 quad_perm:[2,3,0,1] row_mask:0xf bank_mask:0xf bound_ctrl:1
	ds_read_b128 v[32:35], v18 offset:27648
	ds_read_b128 v[24:27], v18 offset:11264
	v_add_f32_dpp v102, v102, v102 row_half_mirror row_mask:0xf bank_mask:0xf bound_ctrl:1
	ds_read_b128 v[36:39], v18 offset:35840
	ds_read2_b32 v[80:81], v2 offset0:192 offset1:208
	v_add_f32_dpp v102, v102, v102 row_mirror row_mask:0xf bank_mask:0xf bound_ctrl:1
	v_pk_fma_f32 v[14:15], v[44:45], v[102:103], v[14:15] op_sel_hi:[1,0,1] neg_lo:[0,1,0] neg_hi:[0,1,0]
	v_pk_fma_f32 v[16:17], v[46:47], v[102:103], v[16:17] op_sel_hi:[1,0,1] neg_lo:[0,1,0] neg_hi:[0,1,0]
	v_add_f32_dpp v114, v112, v112 row_mirror row_mask:0xf bank_mask:0x3 bound_ctrl:1
	v_add_f32_dpp v114, v113, v113 row_mirror row_mask:0xf bank_mask:0xc bound_ctrl:1
	s_waitcnt lgkmcnt(7)
	v_pk_mul_f32 v[104:105], v[14:15], v[60:61]
	v_pk_mul_f32 v[106:107], v[14:15], v[56:57]
	v_pk_fma_f32 v[104:105], v[16:17], v[62:63], v[104:105]
	v_pk_fma_f32 v[106:107], v[16:17], v[58:59], v[106:107]
	v_add_f32_e32 v102, v104, v105
	v_pk_fma_f32 v[14:15], v[72:73], v[92:93], v[14:15] op_sel:[0,1,0]
	v_add_f32_e32 v112, v106, v107
	v_add_f32_dpp v102, v102, v102 quad_perm:[1,0,3,2] row_mask:0xf bank_mask:0xf bound_ctrl:1
	v_pk_fma_f32 v[16:17], v[74:75], v[92:93], v[16:17] op_sel:[0,1,0]
	ds_read_b128 v[40:43], v18 offset:3328
	v_add_f32_dpp v102, v102, v102 quad_perm:[2,3,0,1] row_mask:0xf bank_mask:0xf bound_ctrl:1
	ds_read_b128 v[52:55], v18 offset:27904
	ds_read_b128 v[44:47], v18 offset:11520
	v_add_f32_dpp v102, v102, v102 row_half_mirror row_mask:0xf bank_mask:0xf bound_ctrl:1
	ds_read_b128 v[56:59], v18 offset:36096
	s_nop 0
	v_add_f32_dpp v102, v102, v102 row_mirror row_mask:0xf bank_mask:0xf bound_ctrl:1
	v_pk_fma_f32 v[14:15], v[64:65], v[102:103], v[14:15] op_sel_hi:[1,0,1] neg_lo:[0,1,0] neg_hi:[0,1,0]
	v_pk_fma_f32 v[16:17], v[66:67], v[102:103], v[16:17] op_sel_hi:[1,0,1] neg_lo:[0,1,0] neg_hi:[0,1,0]
	s_waitcnt lgkmcnt(9)
	v_pk_mul_f32 v[14:15], v[14:15], v[68:69]
	v_pk_mul_f32 v[16:17], v[16:17], v[70:71]
	s_waitcnt lgkmcnt(6)
	v_pk_mul_f32 v[104:105], v[14:15], v[20:21]
	v_pk_mul_f32 v[106:107], v[14:15], v[76:77]
	v_pk_fma_f32 v[104:105], v[16:17], v[22:23], v[104:105]
	v_pk_fma_f32 v[106:107], v[16:17], v[78:79], v[106:107]
	v_add_f32_e32 v102, v104, v105
	s_waitcnt lgkmcnt(4)
	v_pk_fma_f32 v[14:15], v[32:33], v[80:81], v[14:15] op_sel_hi:[1,0,1]
	v_add_f32_e32 v113, v106, v107
	v_add_f32_dpp v102, v102, v102 quad_perm:[1,0,3,2] row_mask:0xf bank_mask:0xf bound_ctrl:1
	v_pk_fma_f32 v[16:17], v[34:35], v[80:81], v[16:17] op_sel_hi:[1,0,1]
	ds_read_b128 v[60:63], v18 offset:3584
	v_add_f32_dpp v102, v102, v102 quad_perm:[2,3,0,1] row_mask:0xf bank_mask:0xf bound_ctrl:1
	ds_read_b128 v[72:75], v18 offset:28160
	ds_read_b128 v[64:67], v18 offset:11776
	v_add_f32_dpp v102, v102, v102 row_half_mirror row_mask:0xf bank_mask:0xf bound_ctrl:1
	ds_read_b128 v[76:79], v18 offset:36352
	ds_read2_b32 v[92:93], v2 offset0:224 offset1:240
	v_add_f32_dpp v102, v102, v102 row_mirror row_mask:0xf bank_mask:0xf bound_ctrl:1
	v_pk_fma_f32 v[14:15], v[24:25], v[102:103], v[14:15] op_sel_hi:[1,0,1] neg_lo:[0,1,0] neg_hi:[0,1,0]
	v_pk_fma_f32 v[16:17], v[26:27], v[102:103], v[16:17] op_sel_hi:[1,0,1] neg_lo:[0,1,0] neg_hi:[0,1,0]
	v_add_f32_dpp v115, v112, v112 row_mirror row_mask:0xf bank_mask:0x3 bound_ctrl:1
	v_add_f32_dpp v115, v113, v113 row_mirror row_mask:0xf bank_mask:0xc bound_ctrl:1
	v_add_f32_dpp v116, v114, v114 row_half_mirror row_mask:0xf bank_mask:0x5 bound_ctrl:1
	s_nop 0
	v_add_f32_dpp v116, v115, v115 row_half_mirror row_mask:0xf bank_mask:0xa bound_ctrl:1
	s_waitcnt lgkmcnt(6)
	v_pk_mul_f32 v[104:105], v[14:15], v[40:41]
	v_pk_mul_f32 v[106:107], v[14:15], v[36:37]
	v_pk_fma_f32 v[104:105], v[16:17], v[42:43], v[104:105]
	v_pk_fma_f32 v[106:107], v[16:17], v[38:39], v[106:107]
	v_add_f32_e32 v102, v104, v105
	v_pk_fma_f32 v[14:15], v[52:53], v[80:81], v[14:15] op_sel:[0,1,0]
	v_add_f32_e32 v112, v106, v107
	v_add_f32_dpp v102, v102, v102 quad_perm:[1,0,3,2] row_mask:0xf bank_mask:0xf bound_ctrl:1
	v_pk_fma_f32 v[16:17], v[54:55], v[80:81], v[16:17] op_sel:[0,1,0]
	ds_read_b128 v[20:23], v18 offset:3840
	v_add_f32_dpp v102, v102, v102 quad_perm:[2,3,0,1] row_mask:0xf bank_mask:0xf bound_ctrl:1
	ds_read_b128 v[32:35], v18 offset:28416
	ds_read_b128 v[24:27], v18 offset:12032
	v_add_f32_dpp v102, v102, v102 row_half_mirror row_mask:0xf bank_mask:0xf bound_ctrl:1
	ds_read_b128 v[36:39], v18 offset:36608
	ds_read_b128 v[28:31], v18 offset:20224
	v_add_f32_dpp v102, v102, v102 row_mirror row_mask:0xf bank_mask:0xf bound_ctrl:1
	v_pk_fma_f32 v[14:15], v[44:45], v[102:103], v[14:15] op_sel_hi:[1,0,1] neg_lo:[0,1,0] neg_hi:[0,1,0]
	v_pk_fma_f32 v[16:17], v[46:47], v[102:103], v[16:17] op_sel_hi:[1,0,1] neg_lo:[0,1,0] neg_hi:[0,1,0]
	s_waitcnt lgkmcnt(7)
	v_pk_mul_f32 v[104:105], v[14:15], v[60:61]
	v_pk_mul_f32 v[106:107], v[14:15], v[56:57]
	v_pk_fma_f32 v[104:105], v[16:17], v[62:63], v[104:105]
	v_pk_fma_f32 v[106:107], v[16:17], v[58:59], v[106:107]
	v_add_f32_e32 v102, v104, v105
	s_waitcnt lgkmcnt(5)
	v_pk_fma_f32 v[14:15], v[72:73], v[92:93], v[14:15] op_sel_hi:[1,0,1]
	v_add_f32_e32 v113, v106, v107
	v_add_f32_dpp v102, v102, v102 quad_perm:[1,0,3,2] row_mask:0xf bank_mask:0xf bound_ctrl:1
	v_pk_fma_f32 v[16:17], v[74:75], v[92:93], v[16:17] op_sel_hi:[1,0,1]
	ds_read_b128 v[40:43], v18 offset:4096
	v_add_f32_dpp v102, v102, v102 quad_perm:[2,3,0,1] row_mask:0xf bank_mask:0xf bound_ctrl:1
	ds_read_b128 v[52:55], v18 offset:28672
	ds_read_b128 v[44:47], v18 offset:12288
	v_add_f32_dpp v102, v102, v102 row_half_mirror row_mask:0xf bank_mask:0xf bound_ctrl:1
	ds_read_b128 v[56:59], v18 offset:36864
	ds_read2_b32 v[80:81], v3 offset1:16
	v_add_f32_dpp v102, v102, v102 row_mirror row_mask:0xf bank_mask:0xf bound_ctrl:1
	v_pk_fma_f32 v[14:15], v[64:65], v[102:103], v[14:15] op_sel_hi:[1,0,1] neg_lo:[0,1,0] neg_hi:[0,1,0]
	v_pk_fma_f32 v[16:17], v[66:67], v[102:103], v[16:17] op_sel_hi:[1,0,1] neg_lo:[0,1,0] neg_hi:[0,1,0]
	v_add_f32_dpp v114, v112, v112 row_mirror row_mask:0xf bank_mask:0x3 bound_ctrl:1
	v_add_f32_dpp v114, v113, v113 row_mirror row_mask:0xf bank_mask:0xc bound_ctrl:1
	s_waitcnt lgkmcnt(7)
	v_pk_mul_f32 v[104:105], v[14:15], v[20:21]
	v_pk_mul_f32 v[106:107], v[14:15], v[76:77]
	v_pk_fma_f32 v[104:105], v[16:17], v[22:23], v[104:105]
	v_pk_fma_f32 v[106:107], v[16:17], v[78:79], v[106:107]
	v_add_f32_e32 v102, v104, v105
	v_pk_fma_f32 v[14:15], v[32:33], v[92:93], v[14:15] op_sel:[0,1,0]
	v_add_f32_e32 v112, v106, v107
	v_add_f32_dpp v102, v102, v102 quad_perm:[1,0,3,2] row_mask:0xf bank_mask:0xf bound_ctrl:1
	v_pk_fma_f32 v[16:17], v[34:35], v[92:93], v[16:17] op_sel:[0,1,0]
	ds_read_b128 v[60:63], v18 offset:4352
	v_add_f32_dpp v102, v102, v102 quad_perm:[2,3,0,1] row_mask:0xf bank_mask:0xf bound_ctrl:1
	ds_read_b128 v[72:75], v18 offset:28928
	ds_read_b128 v[64:67], v18 offset:12544
	v_add_f32_dpp v102, v102, v102 row_half_mirror row_mask:0xf bank_mask:0xf bound_ctrl:1
	ds_read_b128 v[76:79], v18 offset:37120
	s_nop 0
	v_add_f32_dpp v102, v102, v102 row_mirror row_mask:0xf bank_mask:0xf bound_ctrl:1
	v_pk_fma_f32 v[14:15], v[24:25], v[102:103], v[14:15] op_sel_hi:[1,0,1] neg_lo:[0,1,0] neg_hi:[0,1,0]
	v_pk_fma_f32 v[16:17], v[26:27], v[102:103], v[16:17] op_sel_hi:[1,0,1] neg_lo:[0,1,0] neg_hi:[0,1,0]
	s_waitcnt lgkmcnt(9)
	v_pk_mul_f32 v[14:15], v[14:15], v[28:29]
	v_pk_mul_f32 v[16:17], v[16:17], v[30:31]
	s_waitcnt lgkmcnt(6)
	v_pk_mul_f32 v[104:105], v[14:15], v[40:41]
	v_pk_mul_f32 v[106:107], v[14:15], v[36:37]
	v_pk_fma_f32 v[104:105], v[16:17], v[42:43], v[104:105]
	v_pk_fma_f32 v[106:107], v[16:17], v[38:39], v[106:107]
	v_add_f32_e32 v102, v104, v105
	s_waitcnt lgkmcnt(4)
	v_pk_fma_f32 v[14:15], v[52:53], v[80:81], v[14:15] op_sel_hi:[1,0,1]
	v_add_f32_e32 v113, v106, v107
	v_add_f32_dpp v102, v102, v102 quad_perm:[1,0,3,2] row_mask:0xf bank_mask:0xf bound_ctrl:1
	v_pk_fma_f32 v[16:17], v[54:55], v[80:81], v[16:17] op_sel_hi:[1,0,1]
	ds_read_b128 v[20:23], v18 offset:4608
	v_add_f32_dpp v102, v102, v102 quad_perm:[2,3,0,1] row_mask:0xf bank_mask:0xf bound_ctrl:1
	ds_read_b128 v[32:35], v18 offset:29184
	ds_read_b128 v[24:27], v18 offset:12800
	v_add_f32_dpp v102, v102, v102 row_half_mirror row_mask:0xf bank_mask:0xf bound_ctrl:1
	ds_read_b128 v[36:39], v18 offset:37376
	ds_read2_b32 v[92:93], v3 offset0:32 offset1:48
	v_add_f32_dpp v102, v102, v102 row_mirror row_mask:0xf bank_mask:0xf bound_ctrl:1
	v_pk_fma_f32 v[14:15], v[44:45], v[102:103], v[14:15] op_sel_hi:[1,0,1] neg_lo:[0,1,0] neg_hi:[0,1,0]
	v_pk_fma_f32 v[16:17], v[46:47], v[102:103], v[16:17] op_sel_hi:[1,0,1] neg_lo:[0,1,0] neg_hi:[0,1,0]
	v_add_f32_dpp v115, v112, v112 row_mirror row_mask:0xf bank_mask:0x3 bound_ctrl:1
	v_add_f32_dpp v115, v113, v113 row_mirror row_mask:0xf bank_mask:0xc bound_ctrl:1
	v_add_f32_dpp v117, v114, v114 row_half_mirror row_mask:0xf bank_mask:0x5 bound_ctrl:1
	s_nop 0
	v_add_f32_dpp v117, v115, v115 row_half_mirror row_mask:0xf bank_mask:0xa bound_ctrl:1
	v_add_f32_dpp v120, v116, v116 quad_perm:[2,3,0,1] row_mask:0xf bank_mask:0xf bound_ctrl:1
	s_nop 0
	v_add_f32_dpp v121, v117, v117 quad_perm:[2,3,0,1] row_mask:0xf bank_mask:0xf bound_ctrl:1
	s_waitcnt lgkmcnt(6)
	v_pk_mul_f32 v[104:105], v[14:15], v[60:61]
	v_pk_mul_f32 v[106:107], v[14:15], v[56:57]
	v_pk_fma_f32 v[104:105], v[16:17], v[62:63], v[104:105]
	v_pk_fma_f32 v[106:107], v[16:17], v[58:59], v[106:107]
	v_add_f32_e32 v102, v104, v105
	v_pk_fma_f32 v[14:15], v[72:73], v[80:81], v[14:15] op_sel:[0,1,0]
	v_add_f32_e32 v112, v106, v107
	v_add_f32_dpp v102, v102, v102 quad_perm:[1,0,3,2] row_mask:0xf bank_mask:0xf bound_ctrl:1
	v_pk_fma_f32 v[16:17], v[74:75], v[80:81], v[16:17] op_sel:[0,1,0]
	ds_read_b128 v[40:43], v18 offset:4864
	v_add_f32_dpp v102, v102, v102 quad_perm:[2,3,0,1] row_mask:0xf bank_mask:0xf bound_ctrl:1
	ds_read_b128 v[52:55], v18 offset:29440
	ds_read_b128 v[44:47], v18 offset:13056
	v_add_f32_dpp v102, v102, v102 row_half_mirror row_mask:0xf bank_mask:0xf bound_ctrl:1
	ds_read_b128 v[56:59], v18 offset:37632
	ds_read_b128 v[48:51], v18 offset:21248
	v_add_f32_dpp v102, v102, v102 row_mirror row_mask:0xf bank_mask:0xf bound_ctrl:1
	v_pk_fma_f32 v[14:15], v[64:65], v[102:103], v[14:15] op_sel_hi:[1,0,1] neg_lo:[0,1,0] neg_hi:[0,1,0]
	v_pk_fma_f32 v[16:17], v[66:67], v[102:103], v[16:17] op_sel_hi:[1,0,1] neg_lo:[0,1,0] neg_hi:[0,1,0]
	v_cndmask_b32_e64 v119, v120, v121, s[14:15]
	v_add_f32_dpp v120, v118, v118 quad_perm:[1,0,3,2] row_mask:0xf bank_mask:0xf bound_ctrl:1
	s_waitcnt lgkmcnt(7)
	v_pk_mul_f32 v[104:105], v[14:15], v[20:21]
	v_pk_mul_f32 v[106:107], v[14:15], v[76:77]
	v_pk_fma_f32 v[104:105], v[16:17], v[22:23], v[104:105]
	v_pk_fma_f32 v[106:107], v[16:17], v[78:79], v[106:107]
	v_add_f32_e32 v102, v104, v105
	s_waitcnt lgkmcnt(5)
	v_pk_fma_f32 v[14:15], v[32:33], v[92:93], v[14:15] op_sel_hi:[1,0,1]
	v_add_f32_e32 v113, v106, v107
	v_add_f32_dpp v102, v102, v102 quad_perm:[1,0,3,2] row_mask:0xf bank_mask:0xf bound_ctrl:1
	v_pk_fma_f32 v[16:17], v[34:35], v[92:93], v[16:17] op_sel_hi:[1,0,1]
	ds_read_b128 v[60:63], v18 offset:5120
	v_add_f32_dpp v102, v102, v102 quad_perm:[2,3,0,1] row_mask:0xf bank_mask:0xf bound_ctrl:1
	ds_read_b128 v[72:75], v18 offset:29696
	ds_read_b128 v[64:67], v18 offset:13312
	v_add_f32_dpp v102, v102, v102 row_half_mirror row_mask:0xf bank_mask:0xf bound_ctrl:1
	ds_read_b128 v[76:79], v18 offset:37888
	ds_read2_b32 v[80:81], v3 offset0:64 offset1:80
	v_add_f32_dpp v102, v102, v102 row_mirror row_mask:0xf bank_mask:0xf bound_ctrl:1
	v_pk_fma_f32 v[14:15], v[24:25], v[102:103], v[14:15] op_sel_hi:[1,0,1] neg_lo:[0,1,0] neg_hi:[0,1,0]
	v_pk_fma_f32 v[16:17], v[26:27], v[102:103], v[16:17] op_sel_hi:[1,0,1] neg_lo:[0,1,0] neg_hi:[0,1,0]
	v_add_f32_dpp v114, v112, v112 row_mirror row_mask:0xf bank_mask:0x3 bound_ctrl:1
	v_add_f32_dpp v114, v113, v113 row_mirror row_mask:0xf bank_mask:0xc bound_ctrl:1
	v_add_f32_dpp v121, v119, v119 quad_perm:[1,0,3,2] row_mask:0xf bank_mask:0xf bound_ctrl:1
	v_cndmask_b32_e64 v122, v120, v121, s[16:17]
	s_waitcnt lgkmcnt(7)
	v_pk_mul_f32 v[104:105], v[14:15], v[40:41]
	v_pk_mul_f32 v[106:107], v[14:15], v[36:37]
	v_pk_fma_f32 v[104:105], v[16:17], v[42:43], v[104:105]
	v_pk_fma_f32 v[106:107], v[16:17], v[38:39], v[106:107]
	v_add_f32_e32 v102, v104, v105
	v_pk_fma_f32 v[14:15], v[52:53], v[92:93], v[14:15] op_sel:[0,1,0]
	v_add_f32_e32 v112, v106, v107
	v_add_f32_dpp v102, v102, v102 quad_perm:[1,0,3,2] row_mask:0xf bank_mask:0xf bound_ctrl:1
	v_pk_fma_f32 v[16:17], v[54:55], v[92:93], v[16:17] op_sel:[0,1,0]
	ds_read_b128 v[20:23], v18 offset:5376
	v_add_f32_dpp v102, v102, v102 quad_perm:[2,3,0,1] row_mask:0xf bank_mask:0xf bound_ctrl:1
	ds_read_b128 v[32:35], v18 offset:29952
	ds_read_b128 v[24:27], v18 offset:13568
	v_add_f32_dpp v102, v102, v102 row_half_mirror row_mask:0xf bank_mask:0xf bound_ctrl:1
	ds_read_b128 v[36:39], v18 offset:38144
	v_bfe_u32 v6, v122, 16, 1
	v_add_f32_dpp v102, v102, v102 row_mirror row_mask:0xf bank_mask:0xf bound_ctrl:1
	v_pk_fma_f32 v[14:15], v[44:45], v[102:103], v[14:15] op_sel_hi:[1,0,1] neg_lo:[0,1,0] neg_hi:[0,1,0]
	v_pk_fma_f32 v[16:17], v[46:47], v[102:103], v[16:17] op_sel_hi:[1,0,1] neg_lo:[0,1,0] neg_hi:[0,1,0]
	s_waitcnt lgkmcnt(9)
	v_pk_mul_f32 v[14:15], v[14:15], v[48:49]
	v_pk_mul_f32 v[16:17], v[16:17], v[50:51]
	v_mul_hi_i32_i24_e32 v5, s44, v89
	v_mul_i32_i24_e32 v4, s44, v89
	s_waitcnt lgkmcnt(6)
	v_pk_mul_f32 v[104:105], v[14:15], v[60:61]
	v_pk_mul_f32 v[106:107], v[14:15], v[56:57]
	v_pk_fma_f32 v[104:105], v[16:17], v[62:63], v[104:105]
	v_pk_fma_f32 v[106:107], v[16:17], v[58:59], v[106:107]
	v_add_f32_e32 v102, v104, v105
	s_waitcnt lgkmcnt(4)
	v_pk_fma_f32 v[14:15], v[72:73], v[80:81], v[14:15] op_sel_hi:[1,0,1]
	v_add_f32_e32 v113, v106, v107
	v_add_f32_dpp v102, v102, v102 quad_perm:[1,0,3,2] row_mask:0xf bank_mask:0xf bound_ctrl:1
	v_pk_fma_f32 v[16:17], v[74:75], v[80:81], v[16:17] op_sel_hi:[1,0,1]
	ds_read_b128 v[40:43], v18 offset:5632
	v_add_f32_dpp v102, v102, v102 quad_perm:[2,3,0,1] row_mask:0xf bank_mask:0xf bound_ctrl:1
	ds_read_b128 v[52:55], v18 offset:30208
	ds_read_b128 v[44:47], v18 offset:13824
	v_add_f32_dpp v102, v102, v102 row_half_mirror row_mask:0xf bank_mask:0xf bound_ctrl:1
	ds_read_b128 v[56:59], v18 offset:38400
	ds_read2_b32 v[92:93], v3 offset0:96 offset1:112
	v_add_f32_dpp v102, v102, v102 row_mirror row_mask:0xf bank_mask:0xf bound_ctrl:1
	v_pk_fma_f32 v[14:15], v[64:65], v[102:103], v[14:15] op_sel_hi:[1,0,1] neg_lo:[0,1,0] neg_hi:[0,1,0]
	v_pk_fma_f32 v[16:17], v[66:67], v[102:103], v[16:17] op_sel_hi:[1,0,1] neg_lo:[0,1,0] neg_hi:[0,1,0]
	v_add_f32_dpp v115, v112, v112 row_mirror row_mask:0xf bank_mask:0x3 bound_ctrl:1
	v_add_f32_dpp v115, v113, v113 row_mirror row_mask:0xf bank_mask:0xc bound_ctrl:1
	v_add_f32_dpp v116, v114, v114 row_half_mirror row_mask:0xf bank_mask:0x5 bound_ctrl:1
	s_nop 0
	v_add_f32_dpp v116, v115, v115 row_half_mirror row_mask:0xf bank_mask:0xa bound_ctrl:1
	v_add3_u32 v6, v122, v6, s3
	v_lshl_add_u64 v[4:5], v[4:5], 1, v[12:13]
	s_waitcnt lgkmcnt(6)
	v_pk_mul_f32 v[104:105], v[14:15], v[20:21]
	v_pk_mul_f32 v[106:107], v[14:15], v[76:77]
	v_pk_fma_f32 v[104:105], v[16:17], v[22:23], v[104:105]
	v_pk_fma_f32 v[106:107], v[16:17], v[78:79], v[106:107]
	v_add_f32_e32 v102, v104, v105
	v_pk_fma_f32 v[14:15], v[32:33], v[80:81], v[14:15] op_sel:[0,1,0]
	v_add_f32_e32 v112, v106, v107
	v_add_f32_dpp v102, v102, v102 quad_perm:[1,0,3,2] row_mask:0xf bank_mask:0xf bound_ctrl:1
	v_pk_fma_f32 v[16:17], v[34:35], v[80:81], v[16:17] op_sel:[0,1,0]
	ds_read_b128 v[60:63], v18 offset:5888
	v_add_f32_dpp v102, v102, v102 quad_perm:[2,3,0,1] row_mask:0xf bank_mask:0xf bound_ctrl:1
	ds_read_b128 v[72:75], v18 offset:30464
	ds_read_b128 v[64:67], v18 offset:14080
	v_add_f32_dpp v102, v102, v102 row_half_mirror row_mask:0xf bank_mask:0xf bound_ctrl:1
	ds_read_b128 v[76:79], v18 offset:38656
	ds_read_b128 v[68:71], v18 offset:22272
	v_add_f32_dpp v102, v102, v102 row_mirror row_mask:0xf bank_mask:0xf bound_ctrl:1
	v_pk_fma_f32 v[14:15], v[24:25], v[102:103], v[14:15] op_sel_hi:[1,0,1] neg_lo:[0,1,0] neg_hi:[0,1,0]
	v_pk_fma_f32 v[16:17], v[26:27], v[102:103], v[16:17] op_sel_hi:[1,0,1] neg_lo:[0,1,0] neg_hi:[0,1,0]
	global_store_short_d16_hi v[4:5], v6, off
	s_waitcnt lgkmcnt(7)
	v_pk_mul_f32 v[104:105], v[14:15], v[40:41]
	v_pk_mul_f32 v[106:107], v[14:15], v[36:37]
	v_pk_fma_f32 v[104:105], v[16:17], v[42:43], v[104:105]
	v_pk_fma_f32 v[106:107], v[16:17], v[38:39], v[106:107]
	v_add_f32_e32 v102, v104, v105
	s_waitcnt lgkmcnt(5)
	v_pk_fma_f32 v[14:15], v[52:53], v[92:93], v[14:15] op_sel_hi:[1,0,1]
	v_add_f32_e32 v113, v106, v107
	v_add_f32_dpp v102, v102, v102 quad_perm:[1,0,3,2] row_mask:0xf bank_mask:0xf bound_ctrl:1
	v_pk_fma_f32 v[16:17], v[54:55], v[92:93], v[16:17] op_sel_hi:[1,0,1]
	ds_read_b128 v[20:23], v18 offset:6144
	v_add_f32_dpp v102, v102, v102 quad_perm:[2,3,0,1] row_mask:0xf bank_mask:0xf bound_ctrl:1
	ds_read_b128 v[32:35], v18 offset:30720
	ds_read_b128 v[24:27], v18 offset:14336
	v_add_f32_dpp v102, v102, v102 row_half_mirror row_mask:0xf bank_mask:0xf bound_ctrl:1
	ds_read_b128 v[36:39], v18 offset:38912
	ds_read2_b32 v[80:81], v3 offset0:128 offset1:144
	v_add_f32_dpp v102, v102, v102 row_mirror row_mask:0xf bank_mask:0xf bound_ctrl:1
	v_pk_fma_f32 v[14:15], v[44:45], v[102:103], v[14:15] op_sel_hi:[1,0,1] neg_lo:[0,1,0] neg_hi:[0,1,0]
	v_pk_fma_f32 v[16:17], v[46:47], v[102:103], v[16:17] op_sel_hi:[1,0,1] neg_lo:[0,1,0] neg_hi:[0,1,0]
	v_add_f32_dpp v114, v112, v112 row_mirror row_mask:0xf bank_mask:0x3 bound_ctrl:1
	v_add_f32_dpp v114, v113, v113 row_mirror row_mask:0xf bank_mask:0xc bound_ctrl:1
	s_waitcnt lgkmcnt(7)
	v_pk_mul_f32 v[104:105], v[14:15], v[60:61]
	v_pk_mul_f32 v[106:107], v[14:15], v[56:57]
	v_pk_fma_f32 v[104:105], v[16:17], v[62:63], v[104:105]
	v_pk_fma_f32 v[106:107], v[16:17], v[58:59], v[106:107]
	v_add_f32_e32 v102, v104, v105
	v_pk_fma_f32 v[14:15], v[72:73], v[92:93], v[14:15] op_sel:[0,1,0]
	v_add_f32_e32 v112, v106, v107
	v_add_f32_dpp v102, v102, v102 quad_perm:[1,0,3,2] row_mask:0xf bank_mask:0xf bound_ctrl:1
	v_pk_fma_f32 v[16:17], v[74:75], v[92:93], v[16:17] op_sel:[0,1,0]
	ds_read_b128 v[40:43], v18 offset:6400
	v_add_f32_dpp v102, v102, v102 quad_perm:[2,3,0,1] row_mask:0xf bank_mask:0xf bound_ctrl:1
	ds_read_b128 v[52:55], v18 offset:30976
	ds_read_b128 v[44:47], v18 offset:14592
	v_add_f32_dpp v102, v102, v102 row_half_mirror row_mask:0xf bank_mask:0xf bound_ctrl:1
	ds_read_b128 v[56:59], v18 offset:39168
	s_nop 0
	v_add_f32_dpp v102, v102, v102 row_mirror row_mask:0xf bank_mask:0xf bound_ctrl:1
	v_pk_fma_f32 v[14:15], v[64:65], v[102:103], v[14:15] op_sel_hi:[1,0,1] neg_lo:[0,1,0] neg_hi:[0,1,0]
	v_pk_fma_f32 v[16:17], v[66:67], v[102:103], v[16:17] op_sel_hi:[1,0,1] neg_lo:[0,1,0] neg_hi:[0,1,0]
	s_waitcnt lgkmcnt(9)
	v_pk_mul_f32 v[14:15], v[14:15], v[68:69]
	v_pk_mul_f32 v[16:17], v[16:17], v[70:71]
	s_waitcnt lgkmcnt(6)
	v_pk_mul_f32 v[104:105], v[14:15], v[20:21]
	v_pk_mul_f32 v[106:107], v[14:15], v[76:77]
	v_pk_fma_f32 v[104:105], v[16:17], v[22:23], v[104:105]
	v_pk_fma_f32 v[106:107], v[16:17], v[78:79], v[106:107]
	v_add_f32_e32 v102, v104, v105
	s_waitcnt lgkmcnt(4)
	v_pk_fma_f32 v[14:15], v[32:33], v[80:81], v[14:15] op_sel_hi:[1,0,1]
	v_add_f32_e32 v113, v106, v107
	v_add_f32_dpp v102, v102, v102 quad_perm:[1,0,3,2] row_mask:0xf bank_mask:0xf bound_ctrl:1
	v_pk_fma_f32 v[16:17], v[34:35], v[80:81], v[16:17] op_sel_hi:[1,0,1]
	ds_read_b128 v[60:63], v18 offset:6656
	v_add_f32_dpp v102, v102, v102 quad_perm:[2,3,0,1] row_mask:0xf bank_mask:0xf bound_ctrl:1
	ds_read_b128 v[72:75], v18 offset:31232
	ds_read_b128 v[64:67], v18 offset:14848
	v_add_f32_dpp v102, v102, v102 row_half_mirror row_mask:0xf bank_mask:0xf bound_ctrl:1
	ds_read_b128 v[76:79], v18 offset:39424
	ds_read2_b32 v[92:93], v3 offset0:160 offset1:176
	v_add_f32_dpp v102, v102, v102 row_mirror row_mask:0xf bank_mask:0xf bound_ctrl:1
	v_pk_fma_f32 v[14:15], v[24:25], v[102:103], v[14:15] op_sel_hi:[1,0,1] neg_lo:[0,1,0] neg_hi:[0,1,0]
	v_pk_fma_f32 v[16:17], v[26:27], v[102:103], v[16:17] op_sel_hi:[1,0,1] neg_lo:[0,1,0] neg_hi:[0,1,0]
	v_add_f32_dpp v115, v112, v112 row_mirror row_mask:0xf bank_mask:0x3 bound_ctrl:1
	v_add_f32_dpp v115, v113, v113 row_mirror row_mask:0xf bank_mask:0xc bound_ctrl:1
	v_add_f32_dpp v117, v114, v114 row_half_mirror row_mask:0xf bank_mask:0x5 bound_ctrl:1
	s_nop 0
	v_add_f32_dpp v117, v115, v115 row_half_mirror row_mask:0xf bank_mask:0xa bound_ctrl:1
	v_add_f32_dpp v120, v116, v116 quad_perm:[2,3,0,1] row_mask:0xf bank_mask:0xf bound_ctrl:1
	s_nop 0
	v_add_f32_dpp v121, v117, v117 quad_perm:[2,3,0,1] row_mask:0xf bank_mask:0xf bound_ctrl:1
	s_waitcnt lgkmcnt(6)
	v_pk_mul_f32 v[104:105], v[14:15], v[40:41]
	v_pk_mul_f32 v[106:107], v[14:15], v[36:37]
	v_pk_fma_f32 v[104:105], v[16:17], v[42:43], v[104:105]
	v_pk_fma_f32 v[106:107], v[16:17], v[38:39], v[106:107]
	v_add_f32_e32 v102, v104, v105
	v_pk_fma_f32 v[14:15], v[52:53], v[80:81], v[14:15] op_sel:[0,1,0]
	v_add_f32_e32 v112, v106, v107
	v_add_f32_dpp v102, v102, v102 quad_perm:[1,0,3,2] row_mask:0xf bank_mask:0xf bound_ctrl:1
	v_pk_fma_f32 v[16:17], v[54:55], v[80:81], v[16:17] op_sel:[0,1,0]
	ds_read_b128 v[20:23], v18 offset:6912
	v_add_f32_dpp v102, v102, v102 quad_perm:[2,3,0,1] row_mask:0xf bank_mask:0xf bound_ctrl:1
	ds_read_b128 v[32:35], v18 offset:31488
	ds_read_b128 v[24:27], v18 offset:15104
	v_add_f32_dpp v102, v102, v102 row_half_mirror row_mask:0xf bank_mask:0xf bound_ctrl:1
	ds_read_b128 v[36:39], v18 offset:39680
	ds_read_b128 v[28:31], v18 offset:23296
	v_add_f32_dpp v102, v102, v102 row_mirror row_mask:0xf bank_mask:0xf bound_ctrl:1
	v_pk_fma_f32 v[14:15], v[44:45], v[102:103], v[14:15] op_sel_hi:[1,0,1] neg_lo:[0,1,0] neg_hi:[0,1,0]
	v_pk_fma_f32 v[16:17], v[46:47], v[102:103], v[16:17] op_sel_hi:[1,0,1] neg_lo:[0,1,0] neg_hi:[0,1,0]
	v_cndmask_b32_e64 v118, v120, v121, s[14:15]
	s_waitcnt lgkmcnt(7)
	v_pk_mul_f32 v[104:105], v[14:15], v[60:61]
	v_pk_mul_f32 v[106:107], v[14:15], v[56:57]
	v_pk_fma_f32 v[104:105], v[16:17], v[62:63], v[104:105]
	v_pk_fma_f32 v[106:107], v[16:17], v[58:59], v[106:107]
	v_add_f32_e32 v102, v104, v105
	s_waitcnt lgkmcnt(5)
	v_pk_fma_f32 v[14:15], v[72:73], v[92:93], v[14:15] op_sel_hi:[1,0,1]
	v_add_f32_e32 v113, v106, v107
	v_add_f32_dpp v102, v102, v102 quad_perm:[1,0,3,2] row_mask:0xf bank_mask:0xf bound_ctrl:1
	v_pk_fma_f32 v[16:17], v[74:75], v[92:93], v[16:17] op_sel_hi:[1,0,1]
	ds_read_b128 v[40:43], v18 offset:7168
	v_add_f32_dpp v102, v102, v102 quad_perm:[2,3,0,1] row_mask:0xf bank_mask:0xf bound_ctrl:1
	ds_read_b128 v[52:55], v18 offset:31744
	ds_read_b128 v[44:47], v18 offset:15360
	v_add_f32_dpp v102, v102, v102 row_half_mirror row_mask:0xf bank_mask:0xf bound_ctrl:1
	ds_read_b128 v[56:59], v18 offset:39936
	ds_read2_b32 v[80:81], v3 offset0:192 offset1:208
	v_add_f32_dpp v102, v102, v102 row_mirror row_mask:0xf bank_mask:0xf bound_ctrl:1
	v_pk_fma_f32 v[14:15], v[64:65], v[102:103], v[14:15] op_sel_hi:[1,0,1] neg_lo:[0,1,0] neg_hi:[0,1,0]
	v_pk_fma_f32 v[16:17], v[66:67], v[102:103], v[16:17] op_sel_hi:[1,0,1] neg_lo:[0,1,0] neg_hi:[0,1,0]
	v_add_f32_dpp v114, v112, v112 row_mirror row_mask:0xf bank_mask:0x3 bound_ctrl:1
	v_add_f32_dpp v114, v113, v113 row_mirror row_mask:0xf bank_mask:0xc bound_ctrl:1
	s_waitcnt lgkmcnt(7)
	v_pk_mul_f32 v[104:105], v[14:15], v[20:21]
	v_pk_mul_f32 v[106:107], v[14:15], v[76:77]
	v_pk_fma_f32 v[104:105], v[16:17], v[22:23], v[104:105]
	v_pk_fma_f32 v[106:107], v[16:17], v[78:79], v[106:107]
	v_add_f32_e32 v102, v104, v105
	v_pk_fma_f32 v[14:15], v[32:33], v[92:93], v[14:15] op_sel:[0,1,0]
	v_add_f32_e32 v112, v106, v107
	v_add_f32_dpp v102, v102, v102 quad_perm:[1,0,3,2] row_mask:0xf bank_mask:0xf bound_ctrl:1
	v_pk_fma_f32 v[16:17], v[34:35], v[92:93], v[16:17] op_sel:[0,1,0]
	ds_read_b128 v[60:63], v18 offset:7424
	v_add_f32_dpp v102, v102, v102 quad_perm:[2,3,0,1] row_mask:0xf bank_mask:0xf bound_ctrl:1
	ds_read_b128 v[72:75], v18 offset:32000
	ds_read_b128 v[64:67], v18 offset:15616
	v_add_f32_dpp v102, v102, v102 row_half_mirror row_mask:0xf bank_mask:0xf bound_ctrl:1
	ds_read_b128 v[76:79], v18 offset:40192
	s_nop 0
	v_add_f32_dpp v102, v102, v102 row_mirror row_mask:0xf bank_mask:0xf bound_ctrl:1
	v_pk_fma_f32 v[14:15], v[24:25], v[102:103], v[14:15] op_sel_hi:[1,0,1] neg_lo:[0,1,0] neg_hi:[0,1,0]
	v_pk_fma_f32 v[16:17], v[26:27], v[102:103], v[16:17] op_sel_hi:[1,0,1] neg_lo:[0,1,0] neg_hi:[0,1,0]
	s_waitcnt lgkmcnt(9)
	v_pk_mul_f32 v[14:15], v[14:15], v[28:29]
	v_pk_mul_f32 v[16:17], v[16:17], v[30:31]
	s_waitcnt lgkmcnt(6)
	v_pk_mul_f32 v[104:105], v[14:15], v[40:41]
	v_pk_mul_f32 v[106:107], v[14:15], v[36:37]
	v_pk_fma_f32 v[104:105], v[16:17], v[42:43], v[104:105]
	v_pk_fma_f32 v[106:107], v[16:17], v[38:39], v[106:107]
	v_add_f32_e32 v102, v104, v105
	s_waitcnt lgkmcnt(4)
	v_pk_fma_f32 v[14:15], v[52:53], v[80:81], v[14:15] op_sel_hi:[1,0,1]
	v_add_f32_e32 v113, v106, v107
	v_add_f32_dpp v102, v102, v102 quad_perm:[1,0,3,2] row_mask:0xf bank_mask:0xf bound_ctrl:1
	v_pk_fma_f32 v[16:17], v[54:55], v[80:81], v[16:17] op_sel_hi:[1,0,1]
	ds_read_b128 v[20:23], v18 offset:7680
	v_add_f32_dpp v102, v102, v102 quad_perm:[2,3,0,1] row_mask:0xf bank_mask:0xf bound_ctrl:1
	ds_read_b128 v[32:35], v18 offset:32256
	ds_read_b128 v[24:27], v18 offset:15872
	v_add_f32_dpp v102, v102, v102 row_half_mirror row_mask:0xf bank_mask:0xf bound_ctrl:1
	ds_read_b128 v[36:39], v18 offset:40448
	ds_read2_b32 v[92:93], v3 offset0:224 offset1:240
	v_add_f32_dpp v102, v102, v102 row_mirror row_mask:0xf bank_mask:0xf bound_ctrl:1
	v_pk_fma_f32 v[14:15], v[44:45], v[102:103], v[14:15] op_sel_hi:[1,0,1] neg_lo:[0,1,0] neg_hi:[0,1,0]
	v_pk_fma_f32 v[16:17], v[46:47], v[102:103], v[16:17] op_sel_hi:[1,0,1] neg_lo:[0,1,0] neg_hi:[0,1,0]
	v_add_f32_dpp v115, v112, v112 row_mirror row_mask:0xf bank_mask:0x3 bound_ctrl:1
	v_add_f32_dpp v115, v113, v113 row_mirror row_mask:0xf bank_mask:0xc bound_ctrl:1
	v_add_f32_dpp v116, v114, v114 row_half_mirror row_mask:0xf bank_mask:0x5 bound_ctrl:1
	s_nop 0
	v_add_f32_dpp v116, v115, v115 row_half_mirror row_mask:0xf bank_mask:0xa bound_ctrl:1
	s_waitcnt lgkmcnt(6)
	v_pk_mul_f32 v[104:105], v[14:15], v[60:61]
	v_pk_mul_f32 v[106:107], v[14:15], v[56:57]
	v_pk_fma_f32 v[104:105], v[16:17], v[62:63], v[104:105]
	v_pk_fma_f32 v[106:107], v[16:17], v[58:59], v[106:107]
	v_add_f32_e32 v102, v104, v105
	v_pk_fma_f32 v[14:15], v[72:73], v[80:81], v[14:15] op_sel:[0,1,0]
	v_add_f32_e32 v112, v106, v107
	v_add_f32_dpp v102, v102, v102 quad_perm:[1,0,3,2] row_mask:0xf bank_mask:0xf bound_ctrl:1
	v_pk_fma_f32 v[16:17], v[74:75], v[80:81], v[16:17] op_sel:[0,1,0]
	ds_read_b128 v[40:43], v18 offset:7936
	v_add_f32_dpp v102, v102, v102 quad_perm:[2,3,0,1] row_mask:0xf bank_mask:0xf bound_ctrl:1
	ds_read_b128 v[52:55], v18 offset:32512
	ds_read_b128 v[44:47], v18 offset:16128
	v_add_f32_dpp v102, v102, v102 row_half_mirror row_mask:0xf bank_mask:0xf bound_ctrl:1
	ds_read_b128 v[56:59], v18 offset:40704
	ds_read_b128 v[48:51], v18 offset:24320
	v_add_f32_dpp v102, v102, v102 row_mirror row_mask:0xf bank_mask:0xf bound_ctrl:1
	v_pk_fma_f32 v[14:15], v[64:65], v[102:103], v[14:15] op_sel_hi:[1,0,1] neg_lo:[0,1,0] neg_hi:[0,1,0]
	v_pk_fma_f32 v[16:17], v[66:67], v[102:103], v[16:17] op_sel_hi:[1,0,1] neg_lo:[0,1,0] neg_hi:[0,1,0]
	s_waitcnt lgkmcnt(7)
	v_pk_mul_f32 v[104:105], v[14:15], v[20:21]
	v_pk_mul_f32 v[106:107], v[14:15], v[76:77]
	v_pk_fma_f32 v[104:105], v[16:17], v[22:23], v[104:105]
	v_pk_fma_f32 v[106:107], v[16:17], v[78:79], v[106:107]
	v_add_f32_e32 v102, v104, v105
	s_waitcnt lgkmcnt(5)
	v_pk_fma_f32 v[14:15], v[32:33], v[92:93], v[14:15] op_sel_hi:[1,0,1]
	v_add_f32_e32 v113, v106, v107
	v_add_f32_dpp v102, v102, v102 quad_perm:[1,0,3,2] row_mask:0xf bank_mask:0xf bound_ctrl:1
	v_pk_fma_f32 v[16:17], v[34:35], v[92:93], v[16:17] op_sel_hi:[1,0,1]
	v_add_f32_dpp v114, v112, v112 row_mirror row_mask:0xf bank_mask:0x3 bound_ctrl:1
	v_add_f32_dpp v102, v102, v102 quad_perm:[2,3,0,1] row_mask:0xf bank_mask:0xf bound_ctrl:1
	v_add_f32_dpp v114, v113, v113 row_mirror row_mask:0xf bank_mask:0xc bound_ctrl:1
	s_nop 0
	v_add_f32_dpp v102, v102, v102 row_half_mirror row_mask:0xf bank_mask:0xf bound_ctrl:1
	s_nop 0
	s_nop 0
	v_add_f32_dpp v102, v102, v102 row_mirror row_mask:0xf bank_mask:0xf bound_ctrl:1
	v_pk_fma_f32 v[14:15], v[24:25], v[102:103], v[14:15] op_sel_hi:[1,0,1] neg_lo:[0,1,0] neg_hi:[0,1,0]
	v_pk_fma_f32 v[16:17], v[26:27], v[102:103], v[16:17] op_sel_hi:[1,0,1] neg_lo:[0,1,0] neg_hi:[0,1,0]
	s_waitcnt lgkmcnt(2)
	v_pk_mul_f32 v[104:105], v[14:15], v[40:41]
	v_pk_mul_f32 v[106:107], v[14:15], v[36:37]
	v_pk_fma_f32 v[104:105], v[16:17], v[42:43], v[104:105]
	v_pk_fma_f32 v[106:107], v[16:17], v[38:39], v[106:107]
	v_add_f32_e32 v102, v104, v105
	v_pk_fma_f32 v[14:15], v[52:53], v[92:93], v[14:15] op_sel:[0,1,0]
	v_add_f32_e32 v112, v106, v107
	v_add_f32_dpp v102, v102, v102 quad_perm:[1,0,3,2] row_mask:0xf bank_mask:0xf bound_ctrl:1
	v_pk_fma_f32 v[16:17], v[54:55], v[92:93], v[16:17] op_sel:[0,1,0]
	s_nop 0
	v_add_f32_dpp v102, v102, v102 quad_perm:[2,3,0,1] row_mask:0xf bank_mask:0xf bound_ctrl:1
	s_nop 0
	s_nop 0
	v_add_f32_dpp v102, v102, v102 row_half_mirror row_mask:0xf bank_mask:0xf bound_ctrl:1
	s_nop 0
	s_nop 0
	v_add_f32_dpp v102, v102, v102 row_mirror row_mask:0xf bank_mask:0xf bound_ctrl:1
	v_pk_fma_f32 v[14:15], v[44:45], v[102:103], v[14:15] op_sel_hi:[1,0,1] neg_lo:[0,1,0] neg_hi:[0,1,0]
	v_pk_fma_f32 v[16:17], v[46:47], v[102:103], v[16:17] op_sel_hi:[1,0,1] neg_lo:[0,1,0] neg_hi:[0,1,0]
	s_waitcnt lgkmcnt(0)
	v_pk_mul_f32 v[14:15], v[14:15], v[48:49]
	v_pk_mul_f32 v[16:17], v[16:17], v[50:51]
	v_pk_mul_f32 v[106:107], v[14:15], v[56:57]
	s_nop 0
	v_pk_fma_f32 v[106:107], v[16:17], v[58:59], v[106:107]
	s_nop 0
	v_add_f32_e32 v113, v106, v107
	v_add_f32_dpp v115, v112, v112 row_mirror row_mask:0xf bank_mask:0x3 bound_ctrl:1
	s_nop 0
	v_add_f32_dpp v115, v113, v113 row_mirror row_mask:0xf bank_mask:0xc bound_ctrl:1
	v_add_f32_dpp v117, v114, v114 row_half_mirror row_mask:0xf bank_mask:0x5 bound_ctrl:1
	s_nop 0
	v_add_f32_dpp v117, v115, v115 row_half_mirror row_mask:0xf bank_mask:0xa bound_ctrl:1
	v_add_f32_dpp v120, v116, v116 quad_perm:[2,3,0,1] row_mask:0xf bank_mask:0xf bound_ctrl:1
	s_nop 0
	v_add_f32_dpp v121, v117, v117 quad_perm:[2,3,0,1] row_mask:0xf bank_mask:0xf bound_ctrl:1
	v_cndmask_b32_e64 v119, v120, v121, s[14:15]
	v_add_f32_dpp v120, v118, v118 quad_perm:[1,0,3,2] row_mask:0xf bank_mask:0xf bound_ctrl:1
	s_nop 0
	v_add_f32_dpp v121, v119, v119 quad_perm:[1,0,3,2] row_mask:0xf bank_mask:0xf bound_ctrl:1
	v_cndmask_b32_e64 v122, v120, v121, s[16:17]
	v_bfe_u32 v7, v122, 16, 1
	v_mul_hi_i32_i24_e32 v9, s44, v94
	v_mul_i32_i24_e32 v8, s44, v94
	v_add3_u32 v7, v122, v7, s3
	v_lshl_add_u64 v[8:9], v[8:9], 1, v[12:13]
	global_store_short_d16_hi v[8:9], v7, off
	s_add_i32 s8, s8, 1
	s_add_i32 s71, s71, 32
	s_cmpk_lg_i32 s8, 0x88
	s_barrier
	s_cbranch_scc0 .LBB0_618

.LBB0_619:
	s_mov_b64 s[60:61], s[84:85]
	s_add_i32 s81, s95, -4
	v_and_b32_e32 v2, 63, v0
	s_load_dwordx2 s[62:63], s[58:59], 0x180
	s_load_dwordx2 s[70:71], s[58:59], 0x190
	s_load_dwordx2 s[72:73], s[58:59], 0x198
	s_load_dwordx2 s[74:75], s[58:59], 0x168
	s_load_dwordx2 s[82:83], s[58:59], 0x188
	s_load_dwordx2 s[84:85], s[58:59], 0x170
	v_and_b32_e32 v3, 31, v2
	v_lshlrev_b32_e32 v3, 2, v3
	v_lshrrev_b32_e32 v7, 5, v2
	v_sub_u32_e32 v8, 1, v7
	v_lshrrev_b32_e32 v4, 3, v2
	v_and_b32_e32 v5, 7, v2
	s_cmp_lg_u32 s50, 0
	s_cselect_b64 vcc, -1, 0
	v_sub_u32_e32 v6, 7, v4
	v_cndmask_b32_e32 v6, v4, v6, vcc
	v_lshlrev_b32_e32 v6, 9, v6
	v_lshl_add_u32 v6, v5, 2, v6
	v_cndmask_b32_e32 v8, v7, v8, vcc
	v_lshl_add_u32 v3, v8, 11, v3
	s_lshl_b32 s0, s81, 11
	v_lshl_add_u32 v7, v7, 10, s0
	v_and_b32_e32 v8, 31, v2
	v_lshl_add_u32 v7, v8, 3, v7
	s_lshl_b32 s0, s81, 9
	s_add_i32 s0, s0, 0xa000
	v_lshl_add_u32 v8, v4, 6, s0
	v_lshl_add_u32 v8, v5, 3, v8
	v_lshlrev_b32_e32 v97, 15, v5
	v_lshl_or_b32 v97, v4, 4, v97
	v_lshlrev_b32_e32 v82, 13, v4
	v_lshl_or_b32 v82, v5, 4, v82
	s_mov_b32 s89, 0xffff0000
	s_lshl_b32 s0, s51, 7
	s_mul_i32 s1, s50, 0x1100000
	s_lshl_b32 s8, s7, 5
	s_waitcnt lgkmcnt(0)
	s_add_u32 s62, s62, s0
	s_addc_u32 s63, s63, 0
	s_add_u32 s74, s74, s0
	s_addc_u32 s75, s75, 0
	s_add_u32 s84, s84, s0
	s_addc_u32 s85, s85, 0
	s_add_u32 s84, s84, s8
	s_addc_u32 s85, s85, 0
	s_add_i32 s0, s0, s1
	s_add_u32 s70, s70, s0
	s_addc_u32 s71, s71, 0
	s_add_u32 s72, s72, s0
	s_addc_u32 s73, s73, 0
	s_add_u32 s82, s82, s0
	s_addc_u32 s83, s83, 0
	s_mov_b32 s8, 0
	s_lshl_b32 s9, s8, 5
	s_lshl_b32 s33, s81, 3
	s_add_i32 s9, s9, s33
	s_lshl_b32 s33, s6, 8
	s_add_i32 s33, s33, 0x8000
	s_lshl_b32 s45, s6, 12
	s_cmp_lt_u32 s8, 8
	s_cselect_b32 s33, s33, s45
	s_cselect_b32 s44, 0, 0x100
	s_movk_i32 s45, 0xff8
	s_cselect_b32 s45, 0xf8, s45
	s_sub_i32 s9, s9, s44
	s_sub_i32 s45, s45, s9
	s_cmp_lg_u32 s50, 0
	s_cselect_b32 s9, s45, s9
	s_add_i32 s33, s33, s9
	s_lshl_b32 s33, s33, 9
	s_cmp_lg_u32 s50, 0
	s_cbranch_scc1 .Lld_bw_p0
	s_add_u32 s0, s82, s33
	s_addc_u32 s1, s83, 0
	global_load_dword v9, v3, s[0:1]
	global_load_dword v10, v3, s[0:1] offset:512
	global_load_dword v11, v3, s[0:1] offset:1024
	global_load_dword v12, v3, s[0:1] offset:1536
	s_add_u32 s0, s62, s33
	s_addc_u32 s1, s63, 0
	global_load_dword v13, v3, s[0:1]
	global_load_dword v14, v3, s[0:1] offset:512
	global_load_dword v15, v3, s[0:1] offset:1024
	global_load_dword v16, v3, s[0:1] offset:1536
	s_add_u32 s0, s70, s33
	s_addc_u32 s1, s71, 0
	global_load_dword v17, v3, s[0:1]
	global_load_dword v18, v3, s[0:1] offset:512
	global_load_dword v19, v3, s[0:1] offset:1024
	global_load_dword v20, v3, s[0:1] offset:1536
	s_add_u32 s0, s72, s33
	s_addc_u32 s1, s73, 0
	global_load_dword v21, v3, s[0:1]
	global_load_dword v22, v3, s[0:1] offset:512
	global_load_dword v23, v3, s[0:1] offset:1024
	global_load_dword v24, v3, s[0:1] offset:1536
	s_add_u32 s0, s74, s33
	s_addc_u32 s1, s75, 0
	global_load_dword v25, v3, s[0:1]
	global_load_dword v26, v3, s[0:1] offset:512
	global_load_dword v27, v3, s[0:1] offset:1024
	global_load_dword v28, v3, s[0:1] offset:1536
	s_add_u32 s0, s84, s33
	s_addc_u32 s1, s85, 0
	global_load_dword v29, v6, s[0:1]
	s_branch .Lld_ldone_p0
.Lld_bw_p0:
	s_add_u32 s0, s82, s33
	s_addc_u32 s1, s83, 0
	global_load_dword v9, v3, s[0:1] offset:1536
	global_load_dword v10, v3, s[0:1] offset:1024
	global_load_dword v11, v3, s[0:1] offset:512
	global_load_dword v12, v3, s[0:1]
	s_add_u32 s0, s62, s33
	s_addc_u32 s1, s63, 0
	global_load_dword v13, v3, s[0:1] offset:1536
	global_load_dword v14, v3, s[0:1] offset:1024
	global_load_dword v15, v3, s[0:1] offset:512
	global_load_dword v16, v3, s[0:1]
	s_add_u32 s0, s70, s33
	s_addc_u32 s1, s71, 0
	global_load_dword v17, v3, s[0:1] offset:1536
	global_load_dword v18, v3, s[0:1] offset:1024
	global_load_dword v19, v3, s[0:1] offset:512
	global_load_dword v20, v3, s[0:1]
	s_add_u32 s0, s72, s33
	s_addc_u32 s1, s73, 0
	global_load_dword v21, v3, s[0:1] offset:1536
	global_load_dword v22, v3, s[0:1] offset:1024
	global_load_dword v23, v3, s[0:1] offset:512
	global_load_dword v24, v3, s[0:1]
	s_add_u32 s0, s74, s33
	s_addc_u32 s1, s75, 0
	global_load_dword v25, v3, s[0:1] offset:1536
	global_load_dword v26, v3, s[0:1] offset:1024
	global_load_dword v27, v3, s[0:1] offset:512
	global_load_dword v28, v3, s[0:1]
	s_add_u32 s0, s84, s33
	s_addc_u32 s1, s85, 0
	global_load_dword v29, v6, s[0:1]
.Lld_ldone_p0:
	s_mov_b32 s8, 1
	s_lshl_b32 s9, s8, 5
	s_lshl_b32 s33, s81, 3
	s_add_i32 s9, s9, s33
	s_lshl_b32 s33, s6, 8
	s_add_i32 s33, s33, 0x8000
	s_lshl_b32 s45, s6, 12
	s_cmp_lt_u32 s8, 8
	s_cselect_b32 s33, s33, s45
	s_cselect_b32 s44, 0, 0x100
	s_movk_i32 s45, 0xff8
	s_cselect_b32 s45, 0xf8, s45
	s_sub_i32 s9, s9, s44
	s_sub_i32 s45, s45, s9
	s_cmp_lg_u32 s50, 0
	s_cselect_b32 s9, s45, s9
	s_add_i32 s33, s33, s9
	s_lshl_b32 s33, s33, 9
	s_cmp_lg_u32 s50, 0
	s_cbranch_scc1 .Lld_bw_p1
	s_add_u32 s0, s82, s33
	s_addc_u32 s1, s83, 0
	global_load_dword v98, v3, s[0:1]
	global_load_dword v99, v3, s[0:1] offset:512
	global_load_dword v100, v3, s[0:1] offset:1024
	global_load_dword v101, v3, s[0:1] offset:1536
	s_add_u32 s0, s62, s33
	s_addc_u32 s1, s63, 0
	global_load_dword v102, v3, s[0:1]
	global_load_dword v103, v3, s[0:1] offset:512
	global_load_dword v104, v3, s[0:1] offset:1024
	global_load_dword v105, v3, s[0:1] offset:1536
	s_add_u32 s0, s70, s33
	s_addc_u32 s1, s71, 0
	global_load_dword v106, v3, s[0:1]
	global_load_dword v107, v3, s[0:1] offset:512
	global_load_dword v108, v3, s[0:1] offset:1024
	global_load_dword v109, v3, s[0:1] offset:1536
	s_add_u32 s0, s72, s33
	s_addc_u32 s1, s73, 0
	global_load_dword v110, v3, s[0:1]
	global_load_dword v111, v3, s[0:1] offset:512
	global_load_dword v112, v3, s[0:1] offset:1024
	global_load_dword v113, v3, s[0:1] offset:1536
	s_add_u32 s0, s74, s33
	s_addc_u32 s1, s75, 0
	global_load_dword v114, v3, s[0:1]
	global_load_dword v115, v3, s[0:1] offset:512
	global_load_dword v116, v3, s[0:1] offset:1024
	global_load_dword v117, v3, s[0:1] offset:1536
	s_add_u32 s0, s84, s33
	s_addc_u32 s1, s85, 0
	global_load_dword v118, v6, s[0:1]
	s_branch .Lld_ldone_p1
.Lld_bw_p1:
	s_add_u32 s0, s82, s33
	s_addc_u32 s1, s83, 0
	global_load_dword v98, v3, s[0:1] offset:1536
	global_load_dword v99, v3, s[0:1] offset:1024
	global_load_dword v100, v3, s[0:1] offset:512
	global_load_dword v101, v3, s[0:1]
	s_add_u32 s0, s62, s33
	s_addc_u32 s1, s63, 0
	global_load_dword v102, v3, s[0:1] offset:1536
	global_load_dword v103, v3, s[0:1] offset:1024
	global_load_dword v104, v3, s[0:1] offset:512
	global_load_dword v105, v3, s[0:1]
	s_add_u32 s0, s70, s33
	s_addc_u32 s1, s71, 0
	global_load_dword v106, v3, s[0:1] offset:1536
	global_load_dword v107, v3, s[0:1] offset:1024
	global_load_dword v108, v3, s[0:1] offset:512
	global_load_dword v109, v3, s[0:1]
	s_add_u32 s0, s72, s33
	s_addc_u32 s1, s73, 0
	global_load_dword v110, v3, s[0:1] offset:1536
	global_load_dword v111, v3, s[0:1] offset:1024
	global_load_dword v112, v3, s[0:1] offset:512
	global_load_dword v113, v3, s[0:1]
	s_add_u32 s0, s74, s33
	s_addc_u32 s1, s75, 0
	global_load_dword v114, v3, s[0:1] offset:1536
	global_load_dword v115, v3, s[0:1] offset:1024
	global_load_dword v116, v3, s[0:1] offset:512
	global_load_dword v117, v3, s[0:1]
	s_add_u32 s0, s84, s33
	s_addc_u32 s1, s85, 0
	global_load_dword v118, v6, s[0:1]
.Lld_ldone_p1:
	s_waitcnt vmcnt(21)
	s_mov_b32 s88, 0
	v_add_u32_e32 v83, s88, v7
	v_add_u32_e32 v96, s88, v8
	v_lshlrev_b32_e32 v92, 16, v29
	v_and_b32_e32 v93, s89, v29
	ds_write_b64 v96, v[92:93]
	v_lshlrev_b32_e32 v92, 16, v9
	v_and_b32_e32 v93, s89, v9
	v_mul_f32_e32 v84, 0x3fb8aa3b, v92
	v_mul_f32_e32 v85, 0x3fb8aa3b, v93
	v_lshlrev_b32_e32 v94, 16, v13
	v_and_b32_e32 v95, s89, v13
	ds_write_b64 v83, v[94:95] offset:0
	v_exp_f32_e64 v86, -v84
	v_exp_f32_e64 v87, -v85
	v_exp_f32_e32 v90, v84
	v_exp_f32_e32 v91, v85
	v_lshlrev_b32_e32 v92, 16, v17
	v_and_b32_e32 v93, s89, v17
	v_mul_f32_e32 v92, v92, v90
	v_mul_f32_e32 v93, v93, v91
	ds_write_b64 v83, v[92:93] offset:8192
	ds_write_b64 v83, v[86:87] offset:16384
	v_lshlrev_b32_e32 v94, 16, v21
	v_and_b32_e32 v95, s89, v21
	v_mul_f32_e32 v94, v94, v90
	v_mul_f32_e32 v95, v95, v91
	ds_write_b64 v83, v[94:95] offset:24576
	v_lshlrev_b32_e32 v92, 16, v25
	v_and_b32_e32 v93, s89, v25
	v_mul_f32_e32 v92, v92, v86
	v_mul_f32_e32 v93, v93, v87
	ds_write_b64 v83, v[92:93] offset:32768
	v_lshlrev_b32_e32 v92, 16, v10
	v_and_b32_e32 v93, s89, v10
	v_fmac_f32_e32 v84, 0x3fb8aa3b, v92
	v_fmac_f32_e32 v85, 0x3fb8aa3b, v93
	v_lshlrev_b32_e32 v94, 16, v14
	v_and_b32_e32 v95, s89, v14
	v_mul_f32_e32 v94, v94, v86
	v_mul_f32_e32 v95, v95, v87
	ds_write_b64 v83, v[94:95] offset:256
	v_exp_f32_e64 v88, -v84
	v_exp_f32_e64 v89, -v85
	v_exp_f32_e32 v90, v84
	v_exp_f32_e32 v91, v85
	v_lshlrev_b32_e32 v92, 16, v18
	v_and_b32_e32 v93, s89, v18
	v_mul_f32_e32 v92, v92, v90
	v_mul_f32_e32 v93, v93, v91
	ds_write_b64 v83, v[92:93] offset:8448
	ds_write_b64 v83, v[88:89] offset:16640
	v_lshlrev_b32_e32 v94, 16, v22
	v_and_b32_e32 v95, s89, v22
	v_mul_f32_e32 v94, v94, v90
	v_mul_f32_e32 v95, v95, v91
	ds_write_b64 v83, v[94:95] offset:24832
	v_lshlrev_b32_e32 v92, 16, v26
	v_and_b32_e32 v93, s89, v26
	v_mul_f32_e32 v92, v92, v88
	v_mul_f32_e32 v93, v93, v89
	ds_write_b64 v83, v[92:93] offset:33024
	v_lshlrev_b32_e32 v92, 16, v11
	v_and_b32_e32 v93, s89, v11
	v_fmac_f32_e32 v84, 0x3fb8aa3b, v92
	v_fmac_f32_e32 v85, 0x3fb8aa3b, v93
	v_lshlrev_b32_e32 v94, 16, v15
	v_and_b32_e32 v95, s89, v15
	v_mul_f32_e32 v94, v94, v88
	v_mul_f32_e32 v95, v95, v89
	ds_write_b64 v83, v[94:95] offset:512
	v_exp_f32_e64 v86, -v84
	v_exp_f32_e64 v87, -v85
	v_exp_f32_e32 v90, v84
	v_exp_f32_e32 v91, v85
	v_lshlrev_b32_e32 v92, 16, v19
	v_and_b32_e32 v93, s89, v19
	v_mul_f32_e32 v92, v92, v90
	v_mul_f32_e32 v93, v93, v91
	ds_write_b64 v83, v[92:93] offset:8704
	ds_write_b64 v83, v[86:87] offset:16896
	v_lshlrev_b32_e32 v94, 16, v23
	v_and_b32_e32 v95, s89, v23
	v_mul_f32_e32 v94, v94, v90
	v_mul_f32_e32 v95, v95, v91
	ds_write_b64 v83, v[94:95] offset:25088
	v_lshlrev_b32_e32 v92, 16, v27
	v_and_b32_e32 v93, s89, v27
	v_mul_f32_e32 v92, v92, v86
	v_mul_f32_e32 v93, v93, v87
	ds_write_b64 v83, v[92:93] offset:33280
	v_lshlrev_b32_e32 v92, 16, v12
	v_and_b32_e32 v93, s89, v12
	v_fmac_f32_e32 v84, 0x3fb8aa3b, v92
	v_fmac_f32_e32 v85, 0x3fb8aa3b, v93
	v_lshlrev_b32_e32 v94, 16, v16
	v_and_b32_e32 v95, s89, v16
	v_mul_f32_e32 v94, v94, v86
	v_mul_f32_e32 v95, v95, v87
	ds_write_b64 v83, v[94:95] offset:768
	v_exp_f32_e64 v88, -v84
	v_exp_f32_e64 v89, -v85
	v_exp_f32_e32 v90, v84
	v_exp_f32_e32 v91, v85
	v_lshlrev_b32_e32 v92, 16, v20
	v_and_b32_e32 v93, s89, v20
	v_mul_f32_e32 v92, v92, v90
	v_mul_f32_e32 v93, v93, v91
	ds_write_b64 v83, v[92:93] offset:8960
	ds_write_b64 v83, v[88:89] offset:17152
	v_lshlrev_b32_e32 v94, 16, v24
	v_and_b32_e32 v95, s89, v24
	v_mul_f32_e32 v94, v94, v90
	v_mul_f32_e32 v95, v95, v91
	ds_write_b64 v83, v[94:95] offset:25344
	v_lshlrev_b32_e32 v92, 16, v28
	v_and_b32_e32 v93, s89, v28
	ds_write_b64 v83, v[92:93] offset:33536
	s_mov_b32 s88, 0xa800
	s_mov_b32 s86, 0
	s_waitcnt lgkmcnt(0)
	s_barrier
.Lld_loop:
	s_mov_b32 s52, 0
	s_lshl_b32 s8, s86, 2
	s_add_i32 s8, s8, s81
	s_mul_i32 s8, s8, s79
	s_add_i32 s8, s8, s2
	s_cmp_lg_u32 s57, s2
	s_cbranch_scc1 .Lld_nocvt_a
	s_cmp_lt_u32 s8, 0x6000
	s_cbranch_scc0 .Lld_nocvt_a
	s_mov_b32 s52, 1
	s_lshr_b32 s9, s8, 13
	s_lshl_b32 s9, s9, 3
	s_add_i32 s9, s9, 0xf8
	s_load_dwordx2 s[44:45], s[58:59], s9
	s_bfe_u32 s9, s8, 0x40009
	s_lshl_b32 s9, s9, 22
	s_bfe_u32 s33, s8, 0x40005
	s_lshl_b32 s33, s33, 18
	s_add_i32 s9, s9, s33
	s_and_b32 s33, s8, 31
	s_lshl_b32 s33, s33, 7
	s_add_i32 s9, s9, s33
	s_waitcnt lgkmcnt(0)
	s_add_u32 s44, s44, s68
	s_addc_u32 s45, s45, s69
	s_add_u32 s44, s44, s9
	s_addc_u32 s45, s45, 0
	global_load_dwordx4 v[50:53], v97, s[44:45] nt
	s_add_u32 s44, s44, 0x1000
	s_addc_u32 s45, s45, 0
	global_load_dwordx4 v[54:57], v97, s[44:45] nt
	s_add_u32 s44, s44, 0x1000
	s_addc_u32 s45, s45, 0
	global_load_dwordx4 v[58:61], v97, s[44:45] nt
	s_add_u32 s44, s44, 0x1000
	s_addc_u32 s45, s45, 0
	global_load_dwordx4 v[62:65], v97, s[44:45] nt
	s_add_u32 s44, s44, 0x1000
	s_addc_u32 s45, s45, 0
	global_load_dwordx4 v[66:69], v97, s[44:45] nt
	s_add_u32 s44, s44, 0x1000
	s_addc_u32 s45, s45, 0
	global_load_dwordx4 v[70:73], v97, s[44:45] nt
	s_add_u32 s44, s44, 0x1000
	s_addc_u32 s45, s45, 0
	global_load_dwordx4 v[74:77], v97, s[44:45] nt
	s_add_u32 s44, s44, 0x1000
	s_addc_u32 s45, s45, 0
	global_load_dwordx4 v[78:81], v97, s[44:45] nt
.Lld_nocvt_a:
	s_add_i32 s8, s86, 2
	s_cmp_lt_u32 s8, 0x88
	s_cbranch_scc0 .Lld_noload_a
	s_lshl_b32 s9, s8, 5
	s_lshl_b32 s33, s81, 3
	s_add_i32 s9, s9, s33
	s_lshl_b32 s33, s6, 8
	s_add_i32 s33, s33, 0x8000
	s_lshl_b32 s45, s6, 12
	s_cmp_lt_u32 s8, 8
	s_cselect_b32 s33, s33, s45
	s_cselect_b32 s44, 0, 0x100
	s_movk_i32 s45, 0xff8
	s_cselect_b32 s45, 0xf8, s45
	s_sub_i32 s9, s9, s44
	s_sub_i32 s45, s45, s9
	s_cmp_lg_u32 s50, 0
	s_cselect_b32 s9, s45, s9
	s_add_i32 s33, s33, s9
	s_lshl_b32 s33, s33, 9
	s_cmp_lg_u32 s50, 0
	s_cbranch_scc1 .Lld_bw_a
	s_add_u32 s0, s82, s33
	s_addc_u32 s1, s83, 0
	global_load_dword v9, v3, s[0:1]
	global_load_dword v10, v3, s[0:1] offset:512
	global_load_dword v11, v3, s[0:1] offset:1024
	global_load_dword v12, v3, s[0:1] offset:1536
	s_add_u32 s0, s62, s33
	s_addc_u32 s1, s63, 0
	global_load_dword v13, v3, s[0:1]
	global_load_dword v14, v3, s[0:1] offset:512
	global_load_dword v15, v3, s[0:1] offset:1024
	global_load_dword v16, v3, s[0:1] offset:1536
	s_add_u32 s0, s70, s33
	s_addc_u32 s1, s71, 0
	global_load_dword v17, v3, s[0:1]
	global_load_dword v18, v3, s[0:1] offset:512
	global_load_dword v19, v3, s[0:1] offset:1024
	global_load_dword v20, v3, s[0:1] offset:1536
	s_add_u32 s0, s72, s33
	s_addc_u32 s1, s73, 0
	global_load_dword v21, v3, s[0:1]
	global_load_dword v22, v3, s[0:1] offset:512
	global_load_dword v23, v3, s[0:1] offset:1024
	global_load_dword v24, v3, s[0:1] offset:1536
	s_add_u32 s0, s74, s33
	s_addc_u32 s1, s75, 0
	global_load_dword v25, v3, s[0:1]
	global_load_dword v26, v3, s[0:1] offset:512
	global_load_dword v27, v3, s[0:1] offset:1024
	global_load_dword v28, v3, s[0:1] offset:1536
	s_add_u32 s0, s84, s33
	s_addc_u32 s1, s85, 0
	global_load_dword v29, v6, s[0:1]
	s_branch .Lld_ldone_a

.Lld_ldone_a:
	s_waitcnt vmcnt(21)
	s_branch .Lld_proc_a

.Lld_proc_a:
	s_add_i32 s8, s86, 1
	s_cmp_lt_u32 s8, 0x88
	s_cbranch_scc0 .Lld_noproc_a
	v_add_u32_e32 v83, s88, v7
	v_add_u32_e32 v96, s88, v8
	v_lshlrev_b32_e32 v92, 16, v118
	v_and_b32_e32 v93, s89, v118
	ds_write_b64 v96, v[92:93]
	v_lshlrev_b32_e32 v92, 16, v98
	v_and_b32_e32 v93, s89, v98
	v_mul_f32_e32 v84, 0x3fb8aa3b, v92
	v_mul_f32_e32 v85, 0x3fb8aa3b, v93
	v_lshlrev_b32_e32 v94, 16, v102
	v_and_b32_e32 v95, s89, v102
	ds_write_b64 v83, v[94:95] offset:0
	v_exp_f32_e64 v86, -v84
	v_exp_f32_e64 v87, -v85
	v_exp_f32_e32 v90, v84
	v_exp_f32_e32 v91, v85
	v_lshlrev_b32_e32 v92, 16, v106
	v_and_b32_e32 v93, s89, v106
	v_mul_f32_e32 v92, v92, v90
	v_mul_f32_e32 v93, v93, v91
	ds_write_b64 v83, v[92:93] offset:8192
	ds_write_b64 v83, v[86:87] offset:16384
	v_lshlrev_b32_e32 v94, 16, v110
	v_and_b32_e32 v95, s89, v110
	v_mul_f32_e32 v94, v94, v90
	v_mul_f32_e32 v95, v95, v91
	ds_write_b64 v83, v[94:95] offset:24576
	v_lshlrev_b32_e32 v92, 16, v114
	v_and_b32_e32 v93, s89, v114
	v_mul_f32_e32 v92, v92, v86
	v_mul_f32_e32 v93, v93, v87
	ds_write_b64 v83, v[92:93] offset:32768
	v_lshlrev_b32_e32 v92, 16, v99
	v_and_b32_e32 v93, s89, v99
	v_fmac_f32_e32 v84, 0x3fb8aa3b, v92
	v_fmac_f32_e32 v85, 0x3fb8aa3b, v93
	v_lshlrev_b32_e32 v94, 16, v103
	v_and_b32_e32 v95, s89, v103
	v_mul_f32_e32 v94, v94, v86
	v_mul_f32_e32 v95, v95, v87
	ds_write_b64 v83, v[94:95] offset:256
	v_exp_f32_e64 v88, -v84
	v_exp_f32_e64 v89, -v85
	v_exp_f32_e32 v90, v84
	v_exp_f32_e32 v91, v85
	v_lshlrev_b32_e32 v92, 16, v107
	v_and_b32_e32 v93, s89, v107
	v_mul_f32_e32 v92, v92, v90
	v_mul_f32_e32 v93, v93, v91
	ds_write_b64 v83, v[92:93] offset:8448
	ds_write_b64 v83, v[88:89] offset:16640
	v_lshlrev_b32_e32 v94, 16, v111
	v_and_b32_e32 v95, s89, v111
	v_mul_f32_e32 v94, v94, v90
	v_mul_f32_e32 v95, v95, v91
	ds_write_b64 v83, v[94:95] offset:24832
	v_lshlrev_b32_e32 v92, 16, v115
	v_and_b32_e32 v93, s89, v115
	v_mul_f32_e32 v92, v92, v88
	v_mul_f32_e32 v93, v93, v89
	ds_write_b64 v83, v[92:93] offset:33024
	v_lshlrev_b32_e32 v92, 16, v100
	v_and_b32_e32 v93, s89, v100
	v_fmac_f32_e32 v84, 0x3fb8aa3b, v92
	v_fmac_f32_e32 v85, 0x3fb8aa3b, v93
	v_lshlrev_b32_e32 v94, 16, v104
	v_and_b32_e32 v95, s89, v104
	v_mul_f32_e32 v94, v94, v88
	v_mul_f32_e32 v95, v95, v89
	ds_write_b64 v83, v[94:95] offset:512
	v_exp_f32_e64 v86, -v84
	v_exp_f32_e64 v87, -v85
	v_exp_f32_e32 v90, v84
	v_exp_f32_e32 v91, v85
	v_lshlrev_b32_e32 v92, 16, v108
	v_and_b32_e32 v93, s89, v108
	v_mul_f32_e32 v92, v92, v90
	v_mul_f32_e32 v93, v93, v91
	ds_write_b64 v83, v[92:93] offset:8704
	ds_write_b64 v83, v[86:87] offset:16896
	v_lshlrev_b32_e32 v94, 16, v112
	v_and_b32_e32 v95, s89, v112
	v_mul_f32_e32 v94, v94, v90
	v_mul_f32_e32 v95, v95, v91
	ds_write_b64 v83, v[94:95] offset:25088
	v_lshlrev_b32_e32 v92, 16, v116
	v_and_b32_e32 v93, s89, v116
	v_mul_f32_e32 v92, v92, v86
	v_mul_f32_e32 v93, v93, v87
	ds_write_b64 v83, v[92:93] offset:33280
	v_lshlrev_b32_e32 v92, 16, v101
	v_and_b32_e32 v93, s89, v101
	v_fmac_f32_e32 v84, 0x3fb8aa3b, v92
	v_fmac_f32_e32 v85, 0x3fb8aa3b, v93
	v_lshlrev_b32_e32 v94, 16, v105
	v_and_b32_e32 v95, s89, v105
	v_mul_f32_e32 v94, v94, v86
	v_mul_f32_e32 v95, v95, v87
	ds_write_b64 v83, v[94:95] offset:768
	v_exp_f32_e64 v88, -v84
	v_exp_f32_e64 v89, -v85
	v_exp_f32_e32 v90, v84
	v_exp_f32_e32 v91, v85
	v_lshlrev_b32_e32 v92, 16, v109
	v_and_b32_e32 v93, s89, v109
	v_mul_f32_e32 v92, v92, v90
	v_mul_f32_e32 v93, v93, v91
	ds_write_b64 v83, v[92:93] offset:8960
	ds_write_b64 v83, v[88:89] offset:17152
	v_lshlrev_b32_e32 v94, 16, v113
	v_and_b32_e32 v95, s89, v113
	v_mul_f32_e32 v94, v94, v90
	v_mul_f32_e32 v95, v95, v91
	ds_write_b64 v83, v[94:95] offset:25344
	v_lshlrev_b32_e32 v92, 16, v117
	v_and_b32_e32 v93, s89, v117
	ds_write_b64 v83, v[92:93] offset:33536
.Lld_noproc_a:
	s_cmp_eq_u32 s52, 0
	s_cbranch_scc1 .Lld_nost_a
	s_lshl_b32 s8, s86, 2
	s_add_i32 s8, s8, s81
	s_mul_i32 s8, s8, s79
	s_add_i32 s8, s8, s2
	s_load_dwordx4 s[44:47], s[58:59], 0x268
	s_lshr_b32 s9, s8, 13
	s_bfe_u32 s33, s8, 0x40009
	s_and_b32 s48, s8, 31
	s_lshl_b32 s48, s48, 5
	s_bfe_u32 s49, s8, 0x40005
	s_lshl_b32 s49, s49, 7
	s_lshr_b32 s0, s48, 7
	s_lshl_b32 s0, s0, 8
	s_and_b32 s1, s48, 127
	s_add_i32 s0, s0, s1
	s_cmp_eq_u32 s9, 1
	s_cselect_b32 s1, 128, 0
	s_add_i32 s0, s0, s1
	s_cmp_lt_u32 s9, 2
	s_cselect_b32 s0, s0, s48
	s_cselect_b32 s1, 22, 21
	s_lshl_b32 s0, s0, 11
	s_add_i32 s0, s0, s49
	s_lshl_b32 s33, s33, s1
	s_add_i32 s0, s0, s33
	s_waitcnt lgkmcnt(0)
	s_cmp_lt_u32 s9, 2
	s_cselect_b32 s44, s44, s46
	s_cselect_b32 s45, s45, s47
	s_add_u32 s44, s44, s0
	s_addc_u32 s45, s45, 0
	s_add_u32 s46, s44, 0x1000
	s_addc_u32 s47, s45, 0
	v_cvt_pk_bf16_f32 v88, v50, v54
	v_cvt_pk_bf16_f32 v89, v58, v62
	v_cvt_pk_bf16_f32 v90, v66, v70
	v_cvt_pk_bf16_f32 v91, v74, v78
	global_store_dwordx4 v82, v[88:91], s[44:45]
	v_cvt_pk_bf16_f32 v92, v51, v55
	v_cvt_pk_bf16_f32 v93, v59, v63
	v_cvt_pk_bf16_f32 v94, v67, v71
	v_cvt_pk_bf16_f32 v95, v75, v79
	global_store_dwordx4 v82, v[92:95], s[44:45] offset:2048
	v_cvt_pk_bf16_f32 v88, v52, v56
	v_cvt_pk_bf16_f32 v89, v60, v64
	v_cvt_pk_bf16_f32 v90, v68, v72
	v_cvt_pk_bf16_f32 v91, v76, v80
	global_store_dwordx4 v82, v[88:91], s[46:47]
	v_cvt_pk_bf16_f32 v92, v53, v57
	v_cvt_pk_bf16_f32 v93, v61, v65
	v_cvt_pk_bf16_f32 v94, v69, v73
	v_cvt_pk_bf16_f32 v95, v77, v81
	global_store_dwordx4 v82, v[92:95], s[46:47] offset:2048
.Lld_nost_a:
	s_add_i32 s88, s88, 0xa800
	s_cmp_eq_u32 s88, 0x1f800
	s_cselect_b32 s88, 0, s88
	s_add_i32 s86, s86, 1
	s_waitcnt lgkmcnt(0)
	s_barrier
	s_mov_b32 s52, 0
	s_lshl_b32 s8, s86, 2
	s_add_i32 s8, s8, s81
	s_mul_i32 s8, s8, s79
	s_add_i32 s8, s8, s2
	s_cmp_lg_u32 s57, s2
	s_cbranch_scc1 .Lld_nocvt_b
	s_cmp_lt_u32 s8, 0x6000
	s_cbranch_scc0 .Lld_nocvt_b
	s_mov_b32 s52, 1
	s_lshr_b32 s9, s8, 13
	s_lshl_b32 s9, s9, 3
	s_add_i32 s9, s9, 0xf8
	s_load_dwordx2 s[44:45], s[58:59], s9
	s_bfe_u32 s9, s8, 0x40009
	s_lshl_b32 s9, s9, 22
	s_bfe_u32 s33, s8, 0x40005
	s_lshl_b32 s33, s33, 18
	s_add_i32 s9, s9, s33
	s_and_b32 s33, s8, 31
	s_lshl_b32 s33, s33, 7
	s_add_i32 s9, s9, s33
	s_waitcnt lgkmcnt(0)
	s_add_u32 s44, s44, s68
	s_addc_u32 s45, s45, s69
	s_add_u32 s44, s44, s9
	s_addc_u32 s45, s45, 0
	global_load_dwordx4 v[50:53], v97, s[44:45] nt
	s_add_u32 s44, s44, 0x1000
	s_addc_u32 s45, s45, 0
	global_load_dwordx4 v[54:57], v97, s[44:45] nt
	s_add_u32 s44, s44, 0x1000
	s_addc_u32 s45, s45, 0
	global_load_dwordx4 v[58:61], v97, s[44:45] nt
	s_add_u32 s44, s44, 0x1000
	s_addc_u32 s45, s45, 0
	global_load_dwordx4 v[62:65], v97, s[44:45] nt
	s_add_u32 s44, s44, 0x1000
	s_addc_u32 s45, s45, 0
	global_load_dwordx4 v[66:69], v97, s[44:45] nt
	s_add_u32 s44, s44, 0x1000
	s_addc_u32 s45, s45, 0
	global_load_dwordx4 v[70:73], v97, s[44:45] nt
	s_add_u32 s44, s44, 0x1000
	s_addc_u32 s45, s45, 0
	global_load_dwordx4 v[74:77], v97, s[44:45] nt
	s_add_u32 s44, s44, 0x1000
	s_addc_u32 s45, s45, 0
	global_load_dwordx4 v[78:81], v97, s[44:45] nt
.Lld_nocvt_b:
	s_add_i32 s8, s86, 2
	s_cmp_lt_u32 s8, 0x88
	s_cbranch_scc0 .Lld_noload_b
	s_lshl_b32 s9, s8, 5
	s_lshl_b32 s33, s81, 3
	s_add_i32 s9, s9, s33
	s_lshl_b32 s33, s6, 8
	s_add_i32 s33, s33, 0x8000
	s_lshl_b32 s45, s6, 12
	s_cmp_lt_u32 s8, 8
	s_cselect_b32 s33, s33, s45
	s_cselect_b32 s44, 0, 0x100
	s_movk_i32 s45, 0xff8
	s_cselect_b32 s45, 0xf8, s45
	s_sub_i32 s9, s9, s44
	s_sub_i32 s45, s45, s9
	s_cmp_lg_u32 s50, 0
	s_cselect_b32 s9, s45, s9
	s_add_i32 s33, s33, s9
	s_lshl_b32 s33, s33, 9
	s_cmp_lg_u32 s50, 0
	s_cbranch_scc1 .Lld_bw_b
	s_add_u32 s0, s82, s33
	s_addc_u32 s1, s83, 0
	global_load_dword v98, v3, s[0:1]
	global_load_dword v99, v3, s[0:1] offset:512
	global_load_dword v100, v3, s[0:1] offset:1024
	global_load_dword v101, v3, s[0:1] offset:1536
	s_add_u32 s0, s62, s33
	s_addc_u32 s1, s63, 0
	global_load_dword v102, v3, s[0:1]
	global_load_dword v103, v3, s[0:1] offset:512
	global_load_dword v104, v3, s[0:1] offset:1024
	global_load_dword v105, v3, s[0:1] offset:1536
	s_add_u32 s0, s70, s33
	s_addc_u32 s1, s71, 0
	global_load_dword v106, v3, s[0:1]
	global_load_dword v107, v3, s[0:1] offset:512
	global_load_dword v108, v3, s[0:1] offset:1024
	global_load_dword v109, v3, s[0:1] offset:1536
	s_add_u32 s0, s72, s33
	s_addc_u32 s1, s73, 0
	global_load_dword v110, v3, s[0:1]
	global_load_dword v111, v3, s[0:1] offset:512
	global_load_dword v112, v3, s[0:1] offset:1024
	global_load_dword v113, v3, s[0:1] offset:1536
	s_add_u32 s0, s74, s33
	s_addc_u32 s1, s75, 0
	global_load_dword v114, v3, s[0:1]
	global_load_dword v115, v3, s[0:1] offset:512
	global_load_dword v116, v3, s[0:1] offset:1024
	global_load_dword v117, v3, s[0:1] offset:1536
	s_add_u32 s0, s84, s33
	s_addc_u32 s1, s85, 0
	global_load_dword v118, v6, s[0:1]
	s_branch .Lld_ldone_b

.Lld_proc_b:
	s_add_i32 s8, s86, 1
	s_cmp_lt_u32 s8, 0x88
	s_cbranch_scc0 .Lld_noproc_b
	v_add_u32_e32 v83, s88, v7
	v_add_u32_e32 v96, s88, v8
	v_lshlrev_b32_e32 v92, 16, v29
	v_and_b32_e32 v93, s89, v29
	ds_write_b64 v96, v[92:93]
	v_lshlrev_b32_e32 v92, 16, v9
	v_and_b32_e32 v93, s89, v9
	v_mul_f32_e32 v84, 0x3fb8aa3b, v92
	v_mul_f32_e32 v85, 0x3fb8aa3b, v93
	v_lshlrev_b32_e32 v94, 16, v13
	v_and_b32_e32 v95, s89, v13
	ds_write_b64 v83, v[94:95] offset:0
	v_exp_f32_e64 v86, -v84
	v_exp_f32_e64 v87, -v85
	v_exp_f32_e32 v90, v84
	v_exp_f32_e32 v91, v85
	v_lshlrev_b32_e32 v92, 16, v17
	v_and_b32_e32 v93, s89, v17
	v_mul_f32_e32 v92, v92, v90
	v_mul_f32_e32 v93, v93, v91
	ds_write_b64 v83, v[92:93] offset:8192
	ds_write_b64 v83, v[86:87] offset:16384
	v_lshlrev_b32_e32 v94, 16, v21
	v_and_b32_e32 v95, s89, v21
	v_mul_f32_e32 v94, v94, v90
	v_mul_f32_e32 v95, v95, v91
	ds_write_b64 v83, v[94:95] offset:24576
	v_lshlrev_b32_e32 v92, 16, v25
	v_and_b32_e32 v93, s89, v25
	v_mul_f32_e32 v92, v92, v86
	v_mul_f32_e32 v93, v93, v87
	ds_write_b64 v83, v[92:93] offset:32768
	v_lshlrev_b32_e32 v92, 16, v10
	v_and_b32_e32 v93, s89, v10
	v_fmac_f32_e32 v84, 0x3fb8aa3b, v92
	v_fmac_f32_e32 v85, 0x3fb8aa3b, v93
	v_lshlrev_b32_e32 v94, 16, v14
	v_and_b32_e32 v95, s89, v14
	v_mul_f32_e32 v94, v94, v86
	v_mul_f32_e32 v95, v95, v87
	ds_write_b64 v83, v[94:95] offset:256
	v_exp_f32_e64 v88, -v84
	v_exp_f32_e64 v89, -v85
	v_exp_f32_e32 v90, v84
	v_exp_f32_e32 v91, v85
	v_lshlrev_b32_e32 v92, 16, v18
	v_and_b32_e32 v93, s89, v18
	v_mul_f32_e32 v92, v92, v90
	v_mul_f32_e32 v93, v93, v91
	ds_write_b64 v83, v[92:93] offset:8448
	ds_write_b64 v83, v[88:89] offset:16640
	v_lshlrev_b32_e32 v94, 16, v22
	v_and_b32_e32 v95, s89, v22
	v_mul_f32_e32 v94, v94, v90
	v_mul_f32_e32 v95, v95, v91
	ds_write_b64 v83, v[94:95] offset:24832
	v_lshlrev_b32_e32 v92, 16, v26
	v_and_b32_e32 v93, s89, v26
	v_mul_f32_e32 v92, v92, v88
	v_mul_f32_e32 v93, v93, v89
	ds_write_b64 v83, v[92:93] offset:33024
	v_lshlrev_b32_e32 v92, 16, v11
	v_and_b32_e32 v93, s89, v11
	v_fmac_f32_e32 v84, 0x3fb8aa3b, v92
	v_fmac_f32_e32 v85, 0x3fb8aa3b, v93
	v_lshlrev_b32_e32 v94, 16, v15
	v_and_b32_e32 v95, s89, v15
	v_mul_f32_e32 v94, v94, v88
	v_mul_f32_e32 v95, v95, v89
	ds_write_b64 v83, v[94:95] offset:512
	v_exp_f32_e64 v86, -v84
	v_exp_f32_e64 v87, -v85
	v_exp_f32_e32 v90, v84
	v_exp_f32_e32 v91, v85
	v_lshlrev_b32_e32 v92, 16, v19
	v_and_b32_e32 v93, s89, v19
	v_mul_f32_e32 v92, v92, v90
	v_mul_f32_e32 v93, v93, v91
	ds_write_b64 v83, v[92:93] offset:8704
	ds_write_b64 v83, v[86:87] offset:16896
	v_lshlrev_b32_e32 v94, 16, v23
	v_and_b32_e32 v95, s89, v23
	v_mul_f32_e32 v94, v94, v90
	v_mul_f32_e32 v95, v95, v91
	ds_write_b64 v83, v[94:95] offset:25088
	v_lshlrev_b32_e32 v92, 16, v27
	v_and_b32_e32 v93, s89, v27
	v_mul_f32_e32 v92, v92, v86
	v_mul_f32_e32 v93, v93, v87
	ds_write_b64 v83, v[92:93] offset:33280
	v_lshlrev_b32_e32 v92, 16, v12
	v_and_b32_e32 v93, s89, v12
	v_fmac_f32_e32 v84, 0x3fb8aa3b, v92
	v_fmac_f32_e32 v85, 0x3fb8aa3b, v93
	v_lshlrev_b32_e32 v94, 16, v16
	v_and_b32_e32 v95, s89, v16
	v_mul_f32_e32 v94, v94, v86
	v_mul_f32_e32 v95, v95, v87
	ds_write_b64 v83, v[94:95] offset:768
	v_exp_f32_e64 v88, -v84
	v_exp_f32_e64 v89, -v85
	v_exp_f32_e32 v90, v84
	v_exp_f32_e32 v91, v85
	v_lshlrev_b32_e32 v92, 16, v20
	v_and_b32_e32 v93, s89, v20
	v_mul_f32_e32 v92, v92, v90
	v_mul_f32_e32 v93, v93, v91
	ds_write_b64 v83, v[92:93] offset:8960
	ds_write_b64 v83, v[88:89] offset:17152
	v_lshlrev_b32_e32 v94, 16, v24
	v_and_b32_e32 v95, s89, v24
	v_mul_f32_e32 v94, v94, v90
	v_mul_f32_e32 v95, v95, v91
	ds_write_b64 v83, v[94:95] offset:25344
	v_lshlrev_b32_e32 v92, 16, v28
	v_and_b32_e32 v93, s89, v28
	ds_write_b64 v83, v[92:93] offset:33536

.Lld_nost_b:
	s_add_i32 s88, s88, 0xa800
	s_cmp_eq_u32 s88, 0x1f800
	s_cselect_b32 s88, 0, s88
	s_add_i32 s86, s86, 1
	s_waitcnt lgkmcnt(0)
	s_barrier
	s_cmp_lt_u32 s86, 0x88
	s_cbranch_scc1 .Lld_loop
	s_branch .LBB0_602
